# same as previous plus a 32 KiB skipped pad after the weight-preparation phase (code placement only)
# speedup vs baseline: 1.0060x; 1.0060x over previous
; __device__ __forceinline__ CArgs cargs() { CArgs p = (CArgs)__builtin_amdgcn_kernarg_segment_ptr(); asm volatile("" : "+s"(p)); return p; }
; #define GRID_BAR_T(FIRST) do { XcdBarrier bb; bb.bar = (unsigned*)(cargs()->ws + WS_CTL) + CW_BAR; bb.x = xb_xcc_id(); bb.st = (volatile LAS unsigned*)(lds + MISC_OFF); \
;         xcd_barrier<FIRST>(bb, phase_tid(wv) == 0); } while (0)
; #define GRID_BAR_T(FIRST) do {} while (0)
; __global__ void __launch_bounds__(NTHR, 2) mk_fwd(Args a) {
;     ...
;     if (PM(0) && IN(0)) { phase_convert(cargs(), lds, wv); phase_convert_b(cargs(), lds, wv); }
;     if (IN(0) && IN(2)) GRID_BAR_T(true);
.LBB0_98:
	s_branch .Lpad_lbb0_98_end
	s_nop 0
	s_nop 0
	s_nop 0
	s_nop 0
	s_nop 0
	s_nop 0
	s_nop 0
	s_nop 0
	s_nop 0
	s_nop 0
	s_nop 0
	s_nop 0
	s_nop 0
	s_nop 0
	s_nop 0
	s_nop 0
	s_nop 0
	s_nop 0
	s_nop 0
	s_nop 0
	s_nop 0
	s_nop 0
	s_nop 0
	s_nop 0
	s_nop 0
	s_nop 0
	s_nop 0
	s_nop 0
	s_nop 0
	s_nop 0
	s_nop 0
	s_nop 0
	s_nop 0
	s_nop 0
	s_nop 0
	s_nop 0
	s_nop 0
	s_nop 0
	s_nop 0
	s_nop 0
	s_nop 0
	s_nop 0
	s_nop 0
	s_nop 0
	s_nop 0
	s_nop 0
	s_nop 0
	s_nop 0
	s_nop 0
	s_nop 0
	s_nop 0
	s_nop 0
	s_nop 0
	s_nop 0
	s_nop 0
	s_nop 0
	s_nop 0
	s_nop 0
	s_nop 0
	s_nop 0
	s_nop 0
	s_nop 0
	s_nop 0
	s_nop 0
	s_nop 0
	s_nop 0
	s_nop 0
	s_nop 0
	s_nop 0
	s_nop 0
	s_nop 0
	s_nop 0
	s_nop 0
	s_nop 0
	s_nop 0
	s_nop 0
	s_nop 0
	s_nop 0
	s_nop 0
	s_nop 0
	s_nop 0
	s_nop 0
	s_nop 0
	s_nop 0
	s_nop 0
	s_nop 0
	s_nop 0
	s_nop 0
	s_nop 0
	s_nop 0
	s_nop 0
	s_nop 0
	s_nop 0
	s_nop 0
	s_nop 0
	s_nop 0
	s_nop 0
	s_nop 0
	s_nop 0
	s_nop 0
	s_nop 0
	s_nop 0
	s_nop 0
	s_nop 0
	s_nop 0
	s_nop 0
	s_nop 0
	s_nop 0
	s_nop 0
	s_nop 0
	s_nop 0
	s_nop 0
	s_nop 0
	s_nop 0
	s_nop 0
	s_nop 0
	s_nop 0
	s_nop 0
	s_nop 0
	s_nop 0
	s_nop 0
	s_nop 0
	s_nop 0
	s_nop 0
	s_nop 0
	s_nop 0
	s_nop 0
	s_nop 0
	s_nop 0
	s_nop 0
	s_nop 0
	s_nop 0
	s_nop 0
	s_nop 0
	s_nop 0
	s_nop 0
	s_nop 0
	s_nop 0
	s_nop 0
	s_nop 0
	s_nop 0
	s_nop 0
	s_nop 0
	s_nop 0
	s_nop 0
	s_nop 0
	s_nop 0
	s_nop 0
	s_nop 0
	s_nop 0
	s_nop 0
	s_nop 0
	s_nop 0
	s_nop 0
	s_nop 0
	s_nop 0
	s_nop 0
	s_nop 0
	s_nop 0
	s_nop 0
	s_nop 0
	s_nop 0
	s_nop 0
	s_nop 0
	s_nop 0
	s_nop 0
	s_nop 0
	s_nop 0
	s_nop 0
	s_nop 0
	s_nop 0
	s_nop 0
	s_nop 0
	s_nop 0
	s_nop 0
	s_nop 0
	s_nop 0
	s_nop 0
	s_nop 0
	s_nop 0
	s_nop 0
	s_nop 0
	s_nop 0
	s_nop 0
	s_nop 0
	s_nop 0
	s_nop 0
	s_nop 0
	s_nop 0
	s_nop 0
	s_nop 0
	s_nop 0
	s_nop 0
	s_nop 0
	s_nop 0
	s_nop 0
	s_nop 0
	s_nop 0
	s_nop 0
	s_nop 0
	s_nop 0
	s_nop 0
	s_nop 0
	s_nop 0
	s_nop 0
	s_nop 0
	s_nop 0
	s_nop 0
	s_nop 0
	s_nop 0
	s_nop 0
	s_nop 0
	s_nop 0
	s_nop 0
	s_nop 0
	s_nop 0
	s_nop 0
	s_nop 0
	s_nop 0
	s_nop 0
	s_nop 0
	s_nop 0
	s_nop 0
	s_nop 0
	s_nop 0
	s_nop 0
	s_nop 0
	s_nop 0
	s_nop 0
	s_nop 0
	s_nop 0
	s_nop 0
	s_nop 0
	s_nop 0
	s_nop 0
	s_nop 0
	s_nop 0
	s_nop 0
	s_nop 0
	s_nop 0
	s_nop 0
	s_nop 0
	s_nop 0
	s_nop 0
	s_nop 0
	s_nop 0
	s_nop 0
	s_nop 0
	s_nop 0
	s_nop 0
	s_nop 0
	s_nop 0
	s_nop 0
	s_nop 0
	s_nop 0
	s_nop 0
	s_nop 0
	s_nop 0
	s_nop 0
	s_nop 0
	s_nop 0
	s_nop 0
	s_nop 0
	s_nop 0
	s_nop 0
	s_nop 0
	s_nop 0
	s_nop 0
	s_nop 0
	s_nop 0
	s_nop 0
	s_nop 0
	s_nop 0
	s_nop 0
	s_nop 0
	s_nop 0
	s_nop 0
	s_nop 0
	s_nop 0
	s_nop 0
	s_nop 0
	s_nop 0
	s_nop 0
	s_nop 0
	s_nop 0
	s_nop 0
	s_nop 0
	s_nop 0
	s_nop 0
	s_nop 0
	s_nop 0
	s_nop 0
	s_nop 0
	s_nop 0
	s_nop 0
	s_nop 0
	s_nop 0
	s_nop 0
	s_nop 0
	s_nop 0
	s_nop 0
	s_nop 0
	s_nop 0
	s_nop 0
	s_nop 0
	s_nop 0
	s_nop 0
	s_nop 0
	s_nop 0
	s_nop 0
	s_nop 0
	s_nop 0
	s_nop 0
	s_nop 0
	s_nop 0
	s_nop 0
	s_nop 0
	s_nop 0
	s_nop 0
	s_nop 0
	s_nop 0
	s_nop 0
	s_nop 0
	s_nop 0
	s_nop 0
	s_nop 0
	s_nop 0
	s_nop 0
	s_nop 0
	s_nop 0
	s_nop 0
	s_nop 0
	s_nop 0
	s_nop 0
	s_nop 0
	s_nop 0
	s_nop 0
	s_nop 0
	s_nop 0
	s_nop 0
	s_nop 0
	s_nop 0
	s_nop 0
	s_nop 0
	s_nop 0
	s_nop 0
	s_nop 0
	s_nop 0
	s_nop 0
	s_nop 0
	s_nop 0
	s_nop 0
	s_nop 0
	s_nop 0
	s_nop 0
	s_nop 0
	s_nop 0
	s_nop 0
	s_nop 0
	s_nop 0
	s_nop 0
	s_nop 0
	s_nop 0
	s_nop 0
	s_nop 0
	s_nop 0
	s_nop 0
	s_nop 0
	s_nop 0
	s_nop 0
	s_nop 0
	s_nop 0
	s_nop 0
	s_nop 0
	s_nop 0
	s_nop 0
	s_nop 0
	s_nop 0
	s_nop 0
	s_nop 0
	s_nop 0
	s_nop 0
	s_nop 0
	s_nop 0
	s_nop 0
	s_nop 0
	s_nop 0
	s_nop 0
	s_nop 0
	s_nop 0
	s_nop 0
	s_nop 0
	s_nop 0
	s_nop 0
	s_nop 0
	s_nop 0
	s_nop 0
	s_nop 0
	s_nop 0
	s_nop 0
	s_nop 0
	s_nop 0
	s_nop 0
	s_nop 0
	s_nop 0
	s_nop 0
	s_nop 0
	s_nop 0
	s_nop 0
	s_nop 0
	s_nop 0
	s_nop 0
	s_nop 0
	s_nop 0
	s_nop 0
	s_nop 0
	s_nop 0
	s_nop 0
	s_nop 0
	s_nop 0
	s_nop 0
	s_nop 0
	s_nop 0
	s_nop 0
	s_nop 0
	s_nop 0
	s_nop 0
	s_nop 0
	s_nop 0
	s_nop 0
	s_nop 0
	s_nop 0
	s_nop 0
	s_nop 0
	s_nop 0
	s_nop 0
	s_nop 0
	s_nop 0
	s_nop 0
	s_nop 0
	s_nop 0
	s_nop 0
	s_nop 0
	s_nop 0
	s_nop 0
	s_nop 0
	s_nop 0
	s_nop 0
	s_nop 0
	s_nop 0
	s_nop 0
	s_nop 0
	s_nop 0
	s_nop 0
	s_nop 0
	s_nop 0
	s_nop 0
	s_nop 0
	s_nop 0
	s_nop 0
	s_nop 0
	s_nop 0
	s_nop 0
	s_nop 0
	s_nop 0
	s_nop 0
	s_nop 0
	s_nop 0
	s_nop 0
	s_nop 0
	s_nop 0
	s_nop 0
	s_nop 0
	s_nop 0
	s_nop 0
	s_nop 0
	s_nop 0
	s_nop 0
	s_nop 0
	s_nop 0
	s_nop 0
	s_nop 0
	s_nop 0
	s_nop 0
	s_nop 0
	s_nop 0
	s_nop 0
	s_nop 0
	s_nop 0
	s_nop 0
	s_nop 0
	s_nop 0
	s_nop 0
	s_nop 0
	s_nop 0
	s_nop 0
	s_nop 0
	s_nop 0
	s_nop 0
	s_nop 0
	s_nop 0
	s_nop 0
	s_nop 0
	s_nop 0
	s_nop 0
	s_nop 0
	s_nop 0
	s_nop 0
	s_nop 0
	s_nop 0
	s_nop 0
	s_nop 0
	s_nop 0
	s_nop 0
	s_nop 0
	s_nop 0
	s_nop 0
	s_nop 0
	s_nop 0
	s_nop 0
	s_nop 0
	s_nop 0
	s_nop 0
	s_nop 0
	s_nop 0
	s_nop 0
	s_nop 0
	s_nop 0
	s_nop 0
	s_nop 0
	s_nop 0
	s_nop 0
	s_nop 0
	s_nop 0
	s_nop 0
	s_nop 0
	s_nop 0
	s_nop 0
	s_nop 0
	s_nop 0
	s_nop 0
	s_nop 0
	s_nop 0
	s_nop 0
	s_nop 0
	s_nop 0
	s_nop 0
	s_nop 0
	s_nop 0
	s_nop 0
	s_nop 0
	s_nop 0
	s_nop 0
	s_nop 0
	s_nop 0
	s_nop 0
	s_nop 0
	s_nop 0
	s_nop 0
	s_nop 0
	s_nop 0
	s_nop 0
	s_nop 0
	s_nop 0
	s_nop 0
	s_nop 0
	s_nop 0
	s_nop 0
	s_nop 0
	s_nop 0
	s_nop 0
	s_nop 0
	s_nop 0
	s_nop 0
	s_nop 0
	s_nop 0
	s_nop 0
	s_nop 0
	s_nop 0
	s_nop 0
	s_nop 0
	s_nop 0
	s_nop 0
	s_nop 0
	s_nop 0
	s_nop 0
	s_nop 0
	s_nop 0
	s_nop 0
	s_nop 0
	s_nop 0
	s_nop 0
	s_nop 0
	s_nop 0
	s_nop 0
	s_nop 0
	s_nop 0
	s_nop 0
	s_nop 0
	s_nop 0
	s_nop 0
	s_nop 0
	s_nop 0
	s_nop 0
	s_nop 0
	s_nop 0
	s_nop 0
	s_nop 0
	s_nop 0
	s_nop 0
	s_nop 0
	s_nop 0
	s_nop 0
	s_nop 0
	s_nop 0
	s_nop 0
	s_nop 0
	s_nop 0
	s_nop 0
	s_nop 0
	s_nop 0
	s_nop 0
; __device__ __forceinline__ CArgs cargs() { CArgs p = (CArgs)__builtin_amdgcn_kernarg_segment_ptr(); asm volatile("" : "+s"(p)); return p; }
; #define GRID_BAR_T(FIRST) do { XcdBarrier bb; bb.bar = (unsigned*)(cargs()->ws + WS_CTL) + CW_BAR; bb.x = xb_xcc_id(); bb.st = (volatile LAS unsigned*)(lds + MISC_OFF); \
;         xcd_barrier<FIRST>(bb, phase_tid(wv) == 0); } while (0)
; #define GRID_BAR_T(FIRST) do {} while (0)
; __global__ void __launch_bounds__(NTHR, 2) mk_fwd(Args a) {
;     ...
;     if (PM(0) && IN(0)) { phase_convert(cargs(), lds, wv); phase_convert_b(cargs(), lds, wv); }
;     if (IN(0) && IN(2)) GRID_BAR_T(true);
	s_nop 0
	s_nop 0
	s_nop 0
	s_nop 0
	s_nop 0
	s_nop 0
	s_nop 0
	s_nop 0
	s_nop 0
	s_nop 0
	s_nop 0
	s_nop 0
	s_nop 0
	s_nop 0
	s_nop 0
	s_nop 0
	s_nop 0
	s_nop 0
	s_nop 0
	s_nop 0
	s_nop 0
	s_nop 0
	s_nop 0
	s_nop 0
	s_nop 0
	s_nop 0
	s_nop 0
	s_nop 0
	s_nop 0
	s_nop 0
	s_nop 0
	s_nop 0
	s_nop 0
	s_nop 0
	s_nop 0
	s_nop 0
	s_nop 0
	s_nop 0
	s_nop 0
	s_nop 0
	s_nop 0
	s_nop 0
	s_nop 0
	s_nop 0
	s_nop 0
	s_nop 0
	s_nop 0
	s_nop 0
	s_nop 0
	s_nop 0
	s_nop 0
	s_nop 0
	s_nop 0
	s_nop 0
	s_nop 0
	s_nop 0
	s_nop 0
	s_nop 0
	s_nop 0
	s_nop 0
	s_nop 0
	s_nop 0
	s_nop 0
	s_nop 0
	s_nop 0
	s_nop 0
	s_nop 0
	s_nop 0
	s_nop 0
	s_nop 0
	s_nop 0
	s_nop 0
	s_nop 0
	s_nop 0
	s_nop 0
	s_nop 0
	s_nop 0
	s_nop 0
	s_nop 0
	s_nop 0
	s_nop 0
	s_nop 0
	s_nop 0
	s_nop 0
	s_nop 0
	s_nop 0
	s_nop 0
	s_nop 0
	s_nop 0
	s_nop 0
	s_nop 0
	s_nop 0
	s_nop 0
	s_nop 0
	s_nop 0
	s_nop 0
	s_nop 0
	s_nop 0
	s_nop 0
	s_nop 0
	s_nop 0
	s_nop 0
	s_nop 0
	s_nop 0
	s_nop 0
	s_nop 0
	s_nop 0
	s_nop 0
	s_nop 0
	s_nop 0
	s_nop 0
	s_nop 0
	s_nop 0
	s_nop 0
	s_nop 0
	s_nop 0
	s_nop 0
	s_nop 0
	s_nop 0
	s_nop 0
	s_nop 0
	s_nop 0
	s_nop 0
	s_nop 0
	s_nop 0
	s_nop 0
	s_nop 0
	s_nop 0
	s_nop 0
	s_nop 0
	s_nop 0
	s_nop 0
	s_nop 0
	s_nop 0
	s_nop 0
	s_nop 0
	s_nop 0
	s_nop 0
	s_nop 0
	s_nop 0
	s_nop 0
	s_nop 0
	s_nop 0
	s_nop 0
	s_nop 0
	s_nop 0
	s_nop 0
	s_nop 0
	s_nop 0
	s_nop 0
	s_nop 0
	s_nop 0
	s_nop 0
	s_nop 0
	s_nop 0
	s_nop 0
	s_nop 0
	s_nop 0
	s_nop 0
	s_nop 0
	s_nop 0
	s_nop 0
	s_nop 0
	s_nop 0
	s_nop 0
	s_nop 0
	s_nop 0
	s_nop 0
	s_nop 0
	s_nop 0
	s_nop 0
	s_nop 0
	s_nop 0
	s_nop 0
	s_nop 0
	s_nop 0
	s_nop 0
	s_nop 0
	s_nop 0
	s_nop 0
	s_nop 0
	s_nop 0
	s_nop 0
	s_nop 0
	s_nop 0
	s_nop 0
	s_nop 0
	s_nop 0
	s_nop 0
	s_nop 0
	s_nop 0
	s_nop 0
	s_nop 0
	s_nop 0
	s_nop 0
	s_nop 0
	s_nop 0
	s_nop 0
	s_nop 0
	s_nop 0
	s_nop 0
	s_nop 0
	s_nop 0
	s_nop 0
	s_nop 0
	s_nop 0
	s_nop 0
	s_nop 0
	s_nop 0
	s_nop 0
	s_nop 0
	s_nop 0
	s_nop 0
	s_nop 0
	s_nop 0
	s_nop 0
	s_nop 0
	s_nop 0
	s_nop 0
	s_nop 0
	s_nop 0
	s_nop 0
	s_nop 0
	s_nop 0
	s_nop 0
	s_nop 0
	s_nop 0
	s_nop 0
	s_nop 0
	s_nop 0
	s_nop 0
	s_nop 0
	s_nop 0
	s_nop 0
	s_nop 0
	s_nop 0
	s_nop 0
	s_nop 0
	s_nop 0
	s_nop 0
	s_nop 0
	s_nop 0
	s_nop 0
	s_nop 0
	s_nop 0
	s_nop 0
	s_nop 0
	s_nop 0
	s_nop 0
	s_nop 0
	s_nop 0
	s_nop 0
	s_nop 0
	s_nop 0
	s_nop 0
	s_nop 0
	s_nop 0
	s_nop 0
	s_nop 0
	s_nop 0
	s_nop 0
	s_nop 0
	s_nop 0
	s_nop 0
	s_nop 0
	s_nop 0
	s_nop 0
	s_nop 0
	s_nop 0
	s_nop 0
	s_nop 0
	s_nop 0
	s_nop 0
	s_nop 0
	s_nop 0
	s_nop 0
	s_nop 0
	s_nop 0
	s_nop 0
	s_nop 0
	s_nop 0
	s_nop 0
	s_nop 0
	s_nop 0
	s_nop 0
	s_nop 0
	s_nop 0
	s_nop 0
	s_nop 0
	s_nop 0
	s_nop 0
	s_nop 0
	s_nop 0
	s_nop 0
	s_nop 0
	s_nop 0
	s_nop 0
	s_nop 0
	s_nop 0
	s_nop 0
	s_nop 0
	s_nop 0
	s_nop 0
	s_nop 0
	s_nop 0
	s_nop 0
	s_nop 0
	s_nop 0
	s_nop 0
	s_nop 0
	s_nop 0
	s_nop 0
	s_nop 0
	s_nop 0
	s_nop 0
	s_nop 0
	s_nop 0
	s_nop 0
	s_nop 0
	s_nop 0
	s_nop 0
	s_nop 0
	s_nop 0
	s_nop 0
	s_nop 0
	s_nop 0
	s_nop 0
	s_nop 0
	s_nop 0
	s_nop 0
	s_nop 0
	s_nop 0
	s_nop 0
	s_nop 0
	s_nop 0
	s_nop 0
	s_nop 0
	s_nop 0
	s_nop 0
	s_nop 0
	s_nop 0
	s_nop 0
	s_nop 0
	s_nop 0
	s_nop 0
	s_nop 0
	s_nop 0
	s_nop 0
	s_nop 0
	s_nop 0
	s_nop 0
	s_nop 0
	s_nop 0
	s_nop 0
	s_nop 0
	s_nop 0
	s_nop 0
	s_nop 0
	s_nop 0
	s_nop 0
	s_nop 0
	s_nop 0
	s_nop 0
	s_nop 0
	s_nop 0
	s_nop 0
	s_nop 0
	s_nop 0
	s_nop 0
	s_nop 0
	s_nop 0
	s_nop 0
	s_nop 0
	s_nop 0
	s_nop 0
	s_nop 0
	s_nop 0
	s_nop 0
	s_nop 0
	s_nop 0
	s_nop 0
	s_nop 0
	s_nop 0
	s_nop 0
	s_nop 0
	s_nop 0
	s_nop 0
	s_nop 0
	s_nop 0
	s_nop 0
	s_nop 0
	s_nop 0
	s_nop 0
	s_nop 0
	s_nop 0
	s_nop 0
	s_nop 0
	s_nop 0
	s_nop 0
	s_nop 0
	s_nop 0
	s_nop 0
	s_nop 0
	s_nop 0
	s_nop 0
	s_nop 0
	s_nop 0
	s_nop 0
	s_nop 0
	s_nop 0
	s_nop 0
	s_nop 0
	s_nop 0
	s_nop 0
	s_nop 0
	s_nop 0
	s_nop 0
	s_nop 0
	s_nop 0
	s_nop 0
	s_nop 0
	s_nop 0
	s_nop 0
	s_nop 0
	s_nop 0
	s_nop 0
	s_nop 0
	s_nop 0
	s_nop 0
	s_nop 0
	s_nop 0
	s_nop 0
	s_nop 0
	s_nop 0
	s_nop 0
	s_nop 0
	s_nop 0
	s_nop 0
	s_nop 0
	s_nop 0
	s_nop 0
	s_nop 0
	s_nop 0
	s_nop 0
	s_nop 0
	s_nop 0
	s_nop 0
	s_nop 0
	s_nop 0
	s_nop 0
	s_nop 0
	s_nop 0
	s_nop 0
	s_nop 0
	s_nop 0
	s_nop 0
	s_nop 0
	s_nop 0
	s_nop 0
	s_nop 0
	s_nop 0
	s_nop 0
	s_nop 0
	s_nop 0
	s_nop 0
	s_nop 0
	s_nop 0
	s_nop 0
	s_nop 0
	s_nop 0
	s_nop 0
	s_nop 0
	s_nop 0
	s_nop 0
	s_nop 0
	s_nop 0
	s_nop 0
	s_nop 0
	s_nop 0
	s_nop 0
	s_nop 0
	s_nop 0
	s_nop 0
	s_nop 0
	s_nop 0
	s_nop 0
	s_nop 0
	s_nop 0
	s_nop 0
	s_nop 0
	s_nop 0
	s_nop 0
	s_nop 0
	s_nop 0
	s_nop 0
	s_nop 0
	s_nop 0
	s_nop 0
	s_nop 0
	s_nop 0
	s_nop 0
	s_nop 0
	s_nop 0
	s_nop 0
	s_nop 0
	s_nop 0
	s_nop 0
	s_nop 0
	s_nop 0
	s_nop 0
	s_nop 0
	s_nop 0
	s_nop 0
	s_nop 0
	s_nop 0
	s_nop 0
	s_nop 0
	s_nop 0
	s_nop 0
	s_nop 0
	s_nop 0
	s_nop 0
	s_nop 0
	s_nop 0
	s_nop 0
	s_nop 0
	s_nop 0
	s_nop 0
	s_nop 0
	s_nop 0
	s_nop 0
	s_nop 0
	s_nop 0
	s_nop 0
	s_nop 0
	s_nop 0
	s_nop 0
	s_nop 0
	s_nop 0
	s_nop 0
	s_nop 0
	s_nop 0
	s_nop 0
	s_nop 0
	s_nop 0
	s_nop 0
	s_nop 0
	s_nop 0
	s_nop 0
	s_nop 0
	s_nop 0
	s_nop 0
	s_nop 0
	s_nop 0
	s_nop 0
	s_nop 0
	s_nop 0
	s_nop 0
	s_nop 0
	s_nop 0
	s_nop 0
	s_nop 0
	s_nop 0
	s_nop 0
	s_nop 0
	s_nop 0
	s_nop 0
	s_nop 0
	s_nop 0
	s_nop 0
	s_nop 0
	s_nop 0
	s_nop 0
	s_nop 0
	s_nop 0
	s_nop 0
	s_nop 0
	s_nop 0
	s_nop 0
	s_nop 0
	s_nop 0
	s_nop 0
	s_nop 0
	s_nop 0
	s_nop 0
	s_nop 0
	s_nop 0
	s_nop 0
	s_nop 0
	s_nop 0
	s_nop 0
	s_nop 0
	s_nop 0
	s_nop 0
	s_nop 0
	s_nop 0
	s_nop 0
	s_nop 0
	s_nop 0
	s_nop 0
	s_nop 0
	s_nop 0
	s_nop 0
	s_nop 0
	s_nop 0
	s_nop 0
	s_nop 0
	s_nop 0
	s_nop 0
	s_nop 0
	s_nop 0
	s_nop 0
	s_nop 0
	s_nop 0
	s_nop 0
	s_nop 0
	s_nop 0
	s_nop 0
	s_nop 0
	s_nop 0
	s_nop 0
	s_nop 0
	s_nop 0
	s_nop 0
	s_nop 0
	s_nop 0
	s_nop 0
; __device__ __forceinline__ CArgs cargs() { CArgs p = (CArgs)__builtin_amdgcn_kernarg_segment_ptr(); asm volatile("" : "+s"(p)); return p; }
; #define GRID_BAR_T(FIRST) do { XcdBarrier bb; bb.bar = (unsigned*)(cargs()->ws + WS_CTL) + CW_BAR; bb.x = xb_xcc_id(); bb.st = (volatile LAS unsigned*)(lds + MISC_OFF); \
;         xcd_barrier<FIRST>(bb, phase_tid(wv) == 0); } while (0)
; #define GRID_BAR_T(FIRST) do {} while (0)
; __global__ void __launch_bounds__(NTHR, 2) mk_fwd(Args a) {
;     ...
;     if (PM(0) && IN(0)) { phase_convert(cargs(), lds, wv); phase_convert_b(cargs(), lds, wv); }
;     if (IN(0) && IN(2)) GRID_BAR_T(true);
	s_nop 0
	s_nop 0
	s_nop 0
	s_nop 0
	s_nop 0
	s_nop 0
	s_nop 0
	s_nop 0
	s_nop 0
	s_nop 0
	s_nop 0
	s_nop 0
	s_nop 0
	s_nop 0
	s_nop 0
	s_nop 0
	s_nop 0
	s_nop 0
	s_nop 0
	s_nop 0
	s_nop 0
	s_nop 0
	s_nop 0
	s_nop 0
	s_nop 0
	s_nop 0
	s_nop 0
	s_nop 0
	s_nop 0
	s_nop 0
	s_nop 0
	s_nop 0
	s_nop 0
	s_nop 0
	s_nop 0
	s_nop 0
	s_nop 0
	s_nop 0
	s_nop 0
	s_nop 0
	s_nop 0
	s_nop 0
	s_nop 0
	s_nop 0
	s_nop 0
	s_nop 0
	s_nop 0
	s_nop 0
	s_nop 0
	s_nop 0
	s_nop 0
	s_nop 0
	s_nop 0
	s_nop 0
	s_nop 0
	s_nop 0
	s_nop 0
	s_nop 0
	s_nop 0
	s_nop 0
	s_nop 0
	s_nop 0
	s_nop 0
	s_nop 0
	s_nop 0
	s_nop 0
	s_nop 0
	s_nop 0
	s_nop 0
	s_nop 0
	s_nop 0
	s_nop 0
	s_nop 0
	s_nop 0
	s_nop 0
	s_nop 0
	s_nop 0
	s_nop 0
	s_nop 0
	s_nop 0
	s_nop 0
	s_nop 0
	s_nop 0
	s_nop 0
	s_nop 0
	s_nop 0
	s_nop 0
	s_nop 0
	s_nop 0
	s_nop 0
	s_nop 0
	s_nop 0
	s_nop 0
	s_nop 0
	s_nop 0
	s_nop 0
	s_nop 0
	s_nop 0
	s_nop 0
	s_nop 0
	s_nop 0
	s_nop 0
	s_nop 0
	s_nop 0
	s_nop 0
	s_nop 0
	s_nop 0
	s_nop 0
	s_nop 0
	s_nop 0
	s_nop 0
	s_nop 0
	s_nop 0
	s_nop 0
	s_nop 0
	s_nop 0
	s_nop 0
	s_nop 0
	s_nop 0
	s_nop 0
	s_nop 0
	s_nop 0
	s_nop 0
	s_nop 0
	s_nop 0
	s_nop 0
	s_nop 0
	s_nop 0
	s_nop 0
	s_nop 0
	s_nop 0
	s_nop 0
	s_nop 0
	s_nop 0
	s_nop 0
	s_nop 0
	s_nop 0
	s_nop 0
	s_nop 0
	s_nop 0
	s_nop 0
	s_nop 0
	s_nop 0
	s_nop 0
	s_nop 0
	s_nop 0
	s_nop 0
	s_nop 0
	s_nop 0
	s_nop 0
	s_nop 0
	s_nop 0
	s_nop 0
	s_nop 0
	s_nop 0
	s_nop 0
	s_nop 0
	s_nop 0
	s_nop 0
	s_nop 0
	s_nop 0
	s_nop 0
	s_nop 0
	s_nop 0
	s_nop 0
	s_nop 0
	s_nop 0
	s_nop 0
	s_nop 0
	s_nop 0
	s_nop 0
	s_nop 0
	s_nop 0
	s_nop 0
	s_nop 0
	s_nop 0
	s_nop 0
	s_nop 0
	s_nop 0
	s_nop 0
	s_nop 0
	s_nop 0
	s_nop 0
	s_nop 0
	s_nop 0
	s_nop 0
	s_nop 0
	s_nop 0
	s_nop 0
	s_nop 0
	s_nop 0
	s_nop 0
	s_nop 0
	s_nop 0
	s_nop 0
	s_nop 0
	s_nop 0
	s_nop 0
	s_nop 0
	s_nop 0
	s_nop 0
	s_nop 0
	s_nop 0
	s_nop 0
	s_nop 0
	s_nop 0
	s_nop 0
	s_nop 0
	s_nop 0
	s_nop 0
	s_nop 0
	s_nop 0
	s_nop 0
	s_nop 0
	s_nop 0
	s_nop 0
	s_nop 0
	s_nop 0
	s_nop 0
	s_nop 0
	s_nop 0
	s_nop 0
	s_nop 0
	s_nop 0
	s_nop 0
	s_nop 0
	s_nop 0
	s_nop 0
	s_nop 0
	s_nop 0
	s_nop 0
	s_nop 0
	s_nop 0
	s_nop 0
	s_nop 0
	s_nop 0
	s_nop 0
	s_nop 0
	s_nop 0
	s_nop 0
	s_nop 0
	s_nop 0
	s_nop 0
	s_nop 0
	s_nop 0
	s_nop 0
	s_nop 0
	s_nop 0
	s_nop 0
	s_nop 0
	s_nop 0
	s_nop 0
	s_nop 0
	s_nop 0
	s_nop 0
	s_nop 0
	s_nop 0
	s_nop 0
	s_nop 0
	s_nop 0
	s_nop 0
	s_nop 0
	s_nop 0
	s_nop 0
	s_nop 0
	s_nop 0
	s_nop 0
	s_nop 0
	s_nop 0
	s_nop 0
	s_nop 0
	s_nop 0
	s_nop 0
	s_nop 0
	s_nop 0
	s_nop 0
	s_nop 0
	s_nop 0
	s_nop 0
	s_nop 0
	s_nop 0
	s_nop 0
	s_nop 0
	s_nop 0
	s_nop 0
	s_nop 0
	s_nop 0
	s_nop 0
	s_nop 0
	s_nop 0
	s_nop 0
	s_nop 0
	s_nop 0
	s_nop 0
	s_nop 0
	s_nop 0
	s_nop 0
	s_nop 0
	s_nop 0
	s_nop 0
	s_nop 0
	s_nop 0
	s_nop 0
	s_nop 0
	s_nop 0
	s_nop 0
	s_nop 0
	s_nop 0
	s_nop 0
	s_nop 0
	s_nop 0
	s_nop 0
	s_nop 0
	s_nop 0
	s_nop 0
	s_nop 0
	s_nop 0
	s_nop 0
	s_nop 0
	s_nop 0
	s_nop 0
	s_nop 0
	s_nop 0
	s_nop 0
	s_nop 0
	s_nop 0
	s_nop 0
	s_nop 0
	s_nop 0
	s_nop 0
	s_nop 0
	s_nop 0
	s_nop 0
	s_nop 0
	s_nop 0
	s_nop 0
	s_nop 0
	s_nop 0
	s_nop 0
	s_nop 0
	s_nop 0
	s_nop 0
	s_nop 0
	s_nop 0
	s_nop 0
	s_nop 0
	s_nop 0
	s_nop 0
	s_nop 0
	s_nop 0
	s_nop 0
	s_nop 0
	s_nop 0
	s_nop 0
	s_nop 0
	s_nop 0
	s_nop 0
	s_nop 0
	s_nop 0
	s_nop 0
	s_nop 0
	s_nop 0
	s_nop 0
	s_nop 0
	s_nop 0
	s_nop 0
	s_nop 0
	s_nop 0
	s_nop 0
	s_nop 0
	s_nop 0
	s_nop 0
	s_nop 0
	s_nop 0
	s_nop 0
	s_nop 0
	s_nop 0
	s_nop 0
	s_nop 0
	s_nop 0
	s_nop 0
	s_nop 0
	s_nop 0
	s_nop 0
	s_nop 0
	s_nop 0
	s_nop 0
	s_nop 0
	s_nop 0
	s_nop 0
	s_nop 0
	s_nop 0
	s_nop 0
	s_nop 0
	s_nop 0
	s_nop 0
	s_nop 0
	s_nop 0
	s_nop 0
	s_nop 0
	s_nop 0
	s_nop 0
	s_nop 0
	s_nop 0
	s_nop 0
	s_nop 0
	s_nop 0
	s_nop 0
	s_nop 0
	s_nop 0
	s_nop 0
	s_nop 0
	s_nop 0
	s_nop 0
	s_nop 0
	s_nop 0
	s_nop 0
	s_nop 0
	s_nop 0
	s_nop 0
	s_nop 0
	s_nop 0
	s_nop 0
	s_nop 0
	s_nop 0
	s_nop 0
	s_nop 0
	s_nop 0
	s_nop 0
	s_nop 0
	s_nop 0
	s_nop 0
	s_nop 0
	s_nop 0
	s_nop 0
	s_nop 0
	s_nop 0
	s_nop 0
	s_nop 0
	s_nop 0
	s_nop 0
	s_nop 0
	s_nop 0
	s_nop 0
	s_nop 0
	s_nop 0
	s_nop 0
	s_nop 0
	s_nop 0
	s_nop 0
	s_nop 0
	s_nop 0
	s_nop 0
	s_nop 0
	s_nop 0
	s_nop 0
	s_nop 0
	s_nop 0
	s_nop 0
	s_nop 0
	s_nop 0
	s_nop 0
	s_nop 0
	s_nop 0
	s_nop 0
	s_nop 0
	s_nop 0
	s_nop 0
	s_nop 0
	s_nop 0
	s_nop 0
	s_nop 0
	s_nop 0
	s_nop 0
	s_nop 0
	s_nop 0
	s_nop 0
	s_nop 0
	s_nop 0
	s_nop 0
	s_nop 0
	s_nop 0
	s_nop 0
	s_nop 0
	s_nop 0
	s_nop 0
	s_nop 0
	s_nop 0
	s_nop 0
	s_nop 0
	s_nop 0
	s_nop 0
	s_nop 0
	s_nop 0
	s_nop 0
	s_nop 0
	s_nop 0
	s_nop 0
	s_nop 0
	s_nop 0
	s_nop 0
	s_nop 0
	s_nop 0
	s_nop 0
	s_nop 0
	s_nop 0
	s_nop 0
	s_nop 0
	s_nop 0
	s_nop 0
	s_nop 0
	s_nop 0
	s_nop 0
	s_nop 0
	s_nop 0
	s_nop 0
	s_nop 0
	s_nop 0
	s_nop 0
	s_nop 0
	s_nop 0
	s_nop 0
	s_nop 0
	s_nop 0
	s_nop 0
	s_nop 0
	s_nop 0
	s_nop 0
	s_nop 0
	s_nop 0
	s_nop 0
	s_nop 0
	s_nop 0
	s_nop 0
	s_nop 0
	s_nop 0
	s_nop 0
	s_nop 0
	s_nop 0
	s_nop 0
	s_nop 0
	s_nop 0
	s_nop 0
	s_nop 0
	s_nop 0
	s_nop 0
	s_nop 0
	s_nop 0
	s_nop 0
	s_nop 0
	s_nop 0
	s_nop 0
	s_nop 0
	s_nop 0
	s_nop 0
	s_nop 0
	s_nop 0
	s_nop 0
	s_nop 0
	s_nop 0
	s_nop 0
	s_nop 0
	s_nop 0
	s_nop 0
	s_nop 0
	s_nop 0
	s_nop 0
	s_nop 0
	s_nop 0
	s_nop 0
	s_nop 0
	s_nop 0
	s_nop 0
	s_nop 0
	s_nop 0
	s_nop 0
	s_nop 0
	s_nop 0
	s_nop 0
	s_nop 0
	s_nop 0
	s_nop 0
	s_nop 0
	s_nop 0
	s_nop 0
	s_nop 0
	s_nop 0
	s_nop 0
	s_nop 0
	s_nop 0
	s_nop 0
	s_nop 0
	s_nop 0
	s_nop 0
	s_nop 0
	s_nop 0
	s_nop 0
	s_nop 0
	s_nop 0
	s_nop 0
	s_nop 0
	s_nop 0
	s_nop 0
	s_nop 0
	s_nop 0
	s_nop 0
	s_nop 0
	s_nop 0
	s_nop 0
	s_nop 0
	s_nop 0
	s_nop 0
	s_nop 0
	s_nop 0
	s_nop 0
	s_nop 0
	s_nop 0
	s_nop 0
	s_nop 0
	s_nop 0
	s_nop 0
	s_nop 0
	s_nop 0
	s_nop 0
	s_nop 0
	s_nop 0
	s_nop 0
; __device__ __forceinline__ CArgs cargs() { CArgs p = (CArgs)__builtin_amdgcn_kernarg_segment_ptr(); asm volatile("" : "+s"(p)); return p; }
; #define GRID_BAR_T(FIRST) do { XcdBarrier bb; bb.bar = (unsigned*)(cargs()->ws + WS_CTL) + CW_BAR; bb.x = xb_xcc_id(); bb.st = (volatile LAS unsigned*)(lds + MISC_OFF); \
;         xcd_barrier<FIRST>(bb, phase_tid(wv) == 0); } while (0)
; #define GRID_BAR_T(FIRST) do {} while (0)
; __global__ void __launch_bounds__(NTHR, 2) mk_fwd(Args a) {
;     ...
;     if (PM(0) && IN(0)) { phase_convert(cargs(), lds, wv); phase_convert_b(cargs(), lds, wv); }
;     if (IN(0) && IN(2)) GRID_BAR_T(true);
	s_nop 0
	s_nop 0
	s_nop 0
	s_nop 0
	s_nop 0
	s_nop 0
	s_nop 0
	s_nop 0
	s_nop 0
	s_nop 0
	s_nop 0
	s_nop 0
	s_nop 0
	s_nop 0
	s_nop 0
	s_nop 0
	s_nop 0
	s_nop 0
	s_nop 0
	s_nop 0
	s_nop 0
	s_nop 0
	s_nop 0
	s_nop 0
	s_nop 0
	s_nop 0
	s_nop 0
	s_nop 0
	s_nop 0
	s_nop 0
	s_nop 0
	s_nop 0
	s_nop 0
	s_nop 0
	s_nop 0
	s_nop 0
	s_nop 0
	s_nop 0
	s_nop 0
	s_nop 0
	s_nop 0
	s_nop 0
	s_nop 0
	s_nop 0
	s_nop 0
	s_nop 0
	s_nop 0
	s_nop 0
	s_nop 0
	s_nop 0
	s_nop 0
	s_nop 0
	s_nop 0
	s_nop 0
	s_nop 0
	s_nop 0
	s_nop 0
	s_nop 0
	s_nop 0
	s_nop 0
	s_nop 0
	s_nop 0
	s_nop 0
	s_nop 0
	s_nop 0
	s_nop 0
	s_nop 0
	s_nop 0
	s_nop 0
	s_nop 0
	s_nop 0
	s_nop 0
	s_nop 0
	s_nop 0
	s_nop 0
	s_nop 0
	s_nop 0
	s_nop 0
	s_nop 0
	s_nop 0
	s_nop 0
	s_nop 0
	s_nop 0
	s_nop 0
	s_nop 0
	s_nop 0
	s_nop 0
	s_nop 0
	s_nop 0
	s_nop 0
	s_nop 0
	s_nop 0
	s_nop 0
	s_nop 0
	s_nop 0
	s_nop 0
	s_nop 0
	s_nop 0
	s_nop 0
	s_nop 0
	s_nop 0
	s_nop 0
	s_nop 0
	s_nop 0
	s_nop 0
	s_nop 0
	s_nop 0
	s_nop 0
	s_nop 0
	s_nop 0
	s_nop 0
	s_nop 0
	s_nop 0
	s_nop 0
	s_nop 0
	s_nop 0
	s_nop 0
	s_nop 0
	s_nop 0
	s_nop 0
	s_nop 0
	s_nop 0
	s_nop 0
	s_nop 0
	s_nop 0
	s_nop 0
	s_nop 0
	s_nop 0
	s_nop 0
	s_nop 0
	s_nop 0
	s_nop 0
	s_nop 0
	s_nop 0
	s_nop 0
	s_nop 0
	s_nop 0
	s_nop 0
	s_nop 0
	s_nop 0
	s_nop 0
	s_nop 0
	s_nop 0
	s_nop 0
	s_nop 0
	s_nop 0
	s_nop 0
	s_nop 0
	s_nop 0
	s_nop 0
	s_nop 0
	s_nop 0
	s_nop 0
	s_nop 0
	s_nop 0
	s_nop 0
	s_nop 0
	s_nop 0
	s_nop 0
	s_nop 0
	s_nop 0
	s_nop 0
	s_nop 0
	s_nop 0
	s_nop 0
	s_nop 0
	s_nop 0
	s_nop 0
	s_nop 0
	s_nop 0
	s_nop 0
	s_nop 0
	s_nop 0
	s_nop 0
	s_nop 0
	s_nop 0
	s_nop 0
	s_nop 0
	s_nop 0
	s_nop 0
	s_nop 0
	s_nop 0
	s_nop 0
	s_nop 0
	s_nop 0
	s_nop 0
	s_nop 0
	s_nop 0
	s_nop 0
	s_nop 0
	s_nop 0
	s_nop 0
	s_nop 0
	s_nop 0
	s_nop 0
	s_nop 0
	s_nop 0
	s_nop 0
	s_nop 0
	s_nop 0
	s_nop 0
	s_nop 0
	s_nop 0
	s_nop 0
	s_nop 0
	s_nop 0
	s_nop 0
	s_nop 0
	s_nop 0
	s_nop 0
	s_nop 0
	s_nop 0
	s_nop 0
	s_nop 0
	s_nop 0
	s_nop 0
	s_nop 0
	s_nop 0
	s_nop 0
	s_nop 0
	s_nop 0
	s_nop 0
	s_nop 0
	s_nop 0
	s_nop 0
	s_nop 0
	s_nop 0
	s_nop 0
	s_nop 0
	s_nop 0
	s_nop 0
	s_nop 0
	s_nop 0
	s_nop 0
	s_nop 0
	s_nop 0
	s_nop 0
	s_nop 0
	s_nop 0
	s_nop 0
	s_nop 0
	s_nop 0
	s_nop 0
	s_nop 0
	s_nop 0
	s_nop 0
	s_nop 0
	s_nop 0
	s_nop 0
	s_nop 0
	s_nop 0
	s_nop 0
	s_nop 0
	s_nop 0
	s_nop 0
	s_nop 0
	s_nop 0
	s_nop 0
	s_nop 0
	s_nop 0
	s_nop 0
	s_nop 0
	s_nop 0
	s_nop 0
	s_nop 0
	s_nop 0
	s_nop 0
	s_nop 0
	s_nop 0
	s_nop 0
	s_nop 0
	s_nop 0
	s_nop 0
	s_nop 0
	s_nop 0
	s_nop 0
	s_nop 0
	s_nop 0
	s_nop 0
	s_nop 0
	s_nop 0
	s_nop 0
	s_nop 0
	s_nop 0
	s_nop 0
	s_nop 0
	s_nop 0
	s_nop 0
	s_nop 0
	s_nop 0
	s_nop 0
	s_nop 0
	s_nop 0
	s_nop 0
	s_nop 0
	s_nop 0
	s_nop 0
	s_nop 0
	s_nop 0
	s_nop 0
	s_nop 0
	s_nop 0
	s_nop 0
	s_nop 0
	s_nop 0
	s_nop 0
	s_nop 0
	s_nop 0
	s_nop 0
	s_nop 0
	s_nop 0
	s_nop 0
	s_nop 0
	s_nop 0
	s_nop 0
	s_nop 0
	s_nop 0
	s_nop 0
	s_nop 0
	s_nop 0
	s_nop 0
	s_nop 0
	s_nop 0
	s_nop 0
	s_nop 0
	s_nop 0
	s_nop 0
	s_nop 0
	s_nop 0
	s_nop 0
	s_nop 0
	s_nop 0
	s_nop 0
	s_nop 0
	s_nop 0
	s_nop 0
	s_nop 0
	s_nop 0
	s_nop 0
	s_nop 0
	s_nop 0
	s_nop 0
	s_nop 0
	s_nop 0
	s_nop 0
	s_nop 0
	s_nop 0
	s_nop 0
	s_nop 0
	s_nop 0
	s_nop 0
	s_nop 0
	s_nop 0
	s_nop 0
	s_nop 0
	s_nop 0
	s_nop 0
	s_nop 0
	s_nop 0
	s_nop 0
	s_nop 0
	s_nop 0
	s_nop 0
	s_nop 0
	s_nop 0
	s_nop 0
	s_nop 0
	s_nop 0
	s_nop 0
	s_nop 0
	s_nop 0
	s_nop 0
	s_nop 0
	s_nop 0
	s_nop 0
	s_nop 0
	s_nop 0
	s_nop 0
	s_nop 0
	s_nop 0
	s_nop 0
	s_nop 0
	s_nop 0
	s_nop 0
	s_nop 0
	s_nop 0
	s_nop 0
	s_nop 0
	s_nop 0
	s_nop 0
	s_nop 0
	s_nop 0
	s_nop 0
	s_nop 0
	s_nop 0
	s_nop 0
	s_nop 0
	s_nop 0
	s_nop 0
	s_nop 0
	s_nop 0
	s_nop 0
	s_nop 0
	s_nop 0
	s_nop 0
	s_nop 0
	s_nop 0
	s_nop 0
	s_nop 0
	s_nop 0
	s_nop 0
	s_nop 0
	s_nop 0
	s_nop 0
	s_nop 0
	s_nop 0
	s_nop 0
	s_nop 0
	s_nop 0
	s_nop 0
	s_nop 0
	s_nop 0
	s_nop 0
	s_nop 0
	s_nop 0
	s_nop 0
	s_nop 0
	s_nop 0
	s_nop 0
	s_nop 0
	s_nop 0
	s_nop 0
	s_nop 0
	s_nop 0
	s_nop 0
	s_nop 0
	s_nop 0
	s_nop 0
	s_nop 0
	s_nop 0
	s_nop 0
	s_nop 0
	s_nop 0
	s_nop 0
	s_nop 0
	s_nop 0
	s_nop 0
	s_nop 0
	s_nop 0
	s_nop 0
	s_nop 0
	s_nop 0
	s_nop 0
	s_nop 0
	s_nop 0
	s_nop 0
	s_nop 0
	s_nop 0
	s_nop 0
	s_nop 0
	s_nop 0
	s_nop 0
	s_nop 0
	s_nop 0
	s_nop 0
	s_nop 0
	s_nop 0
	s_nop 0
	s_nop 0
	s_nop 0
	s_nop 0
	s_nop 0
	s_nop 0
	s_nop 0
	s_nop 0
	s_nop 0
	s_nop 0
	s_nop 0
	s_nop 0
	s_nop 0
	s_nop 0
	s_nop 0
	s_nop 0
	s_nop 0
	s_nop 0
	s_nop 0
	s_nop 0
	s_nop 0
	s_nop 0
	s_nop 0
	s_nop 0
	s_nop 0
	s_nop 0
	s_nop 0
	s_nop 0
	s_nop 0
	s_nop 0
	s_nop 0
	s_nop 0
	s_nop 0
	s_nop 0
	s_nop 0
	s_nop 0
	s_nop 0
	s_nop 0
	s_nop 0
	s_nop 0
	s_nop 0
	s_nop 0
	s_nop 0
	s_nop 0
	s_nop 0
	s_nop 0
	s_nop 0
	s_nop 0
	s_nop 0
	s_nop 0
	s_nop 0
	s_nop 0
	s_nop 0
	s_nop 0
	s_nop 0
	s_nop 0
	s_nop 0
	s_nop 0
	s_nop 0
	s_nop 0
	s_nop 0
	s_nop 0
	s_nop 0
	s_nop 0
	s_nop 0
	s_nop 0
	s_nop 0
	s_nop 0
	s_nop 0
	s_nop 0
	s_nop 0
	s_nop 0
	s_nop 0
	s_nop 0
	s_nop 0
	s_nop 0
	s_nop 0
	s_nop 0
	s_nop 0
	s_nop 0
	s_nop 0
	s_nop 0
	s_nop 0
	s_nop 0
	s_nop 0
	s_nop 0
	s_nop 0
	s_nop 0
	s_nop 0
	s_nop 0
	s_nop 0
	s_nop 0
	s_nop 0
	s_nop 0
	s_nop 0
	s_nop 0
	s_nop 0
	s_nop 0
	s_nop 0
	s_nop 0
	s_nop 0
	s_nop 0
	s_nop 0
	s_nop 0
	s_nop 0
	s_nop 0
	s_nop 0
	s_nop 0
	s_nop 0
	s_nop 0
	s_nop 0
	s_nop 0
	s_nop 0
	s_nop 0
	s_nop 0
	s_nop 0
	s_nop 0
	s_nop 0
	s_nop 0
	s_nop 0
	s_nop 0
	s_nop 0
	s_nop 0
	s_nop 0
	s_nop 0
	s_nop 0
	s_nop 0
	s_nop 0
	s_nop 0
	s_nop 0
	s_nop 0
	s_nop 0
	s_nop 0
	s_nop 0
	s_nop 0
	s_nop 0
	s_nop 0
	s_nop 0
	s_nop 0
	s_nop 0
	s_nop 0
	s_nop 0
	s_nop 0
	s_nop 0
	s_nop 0
	s_nop 0
	s_nop 0
	s_nop 0
	s_nop 0
	s_nop 0
	s_nop 0
	s_nop 0
	s_nop 0
	s_nop 0
	s_nop 0
	s_nop 0
	s_nop 0
	s_nop 0
	s_nop 0
	s_nop 0
; __device__ __forceinline__ CArgs cargs() { CArgs p = (CArgs)__builtin_amdgcn_kernarg_segment_ptr(); asm volatile("" : "+s"(p)); return p; }
; #define GRID_BAR_T(FIRST) do { XcdBarrier bb; bb.bar = (unsigned*)(cargs()->ws + WS_CTL) + CW_BAR; bb.x = xb_xcc_id(); bb.st = (volatile LAS unsigned*)(lds + MISC_OFF); \
;         xcd_barrier<FIRST>(bb, phase_tid(wv) == 0); } while (0)
; #define GRID_BAR_T(FIRST) do {} while (0)
; __global__ void __launch_bounds__(NTHR, 2) mk_fwd(Args a) {
;     ...
;     if (PM(0) && IN(0)) { phase_convert(cargs(), lds, wv); phase_convert_b(cargs(), lds, wv); }
;     if (IN(0) && IN(2)) GRID_BAR_T(true);
	s_nop 0
	s_nop 0
	s_nop 0
	s_nop 0
	s_nop 0
	s_nop 0
	s_nop 0
	s_nop 0
	s_nop 0
	s_nop 0
	s_nop 0
	s_nop 0
	s_nop 0
	s_nop 0
	s_nop 0
	s_nop 0
	s_nop 0
	s_nop 0
	s_nop 0
	s_nop 0
	s_nop 0
	s_nop 0
	s_nop 0
	s_nop 0
	s_nop 0
	s_nop 0
	s_nop 0
	s_nop 0
	s_nop 0
	s_nop 0
	s_nop 0
	s_nop 0
	s_nop 0
	s_nop 0
	s_nop 0
	s_nop 0
	s_nop 0
	s_nop 0
	s_nop 0
	s_nop 0
	s_nop 0
	s_nop 0
	s_nop 0
	s_nop 0
	s_nop 0
	s_nop 0
	s_nop 0
	s_nop 0
	s_nop 0
	s_nop 0
	s_nop 0
	s_nop 0
	s_nop 0
	s_nop 0
	s_nop 0
	s_nop 0
	s_nop 0
	s_nop 0
	s_nop 0
	s_nop 0
	s_nop 0
	s_nop 0
	s_nop 0
	s_nop 0
	s_nop 0
	s_nop 0
	s_nop 0
	s_nop 0
	s_nop 0
	s_nop 0
	s_nop 0
	s_nop 0
	s_nop 0
	s_nop 0
	s_nop 0
	s_nop 0
	s_nop 0
	s_nop 0
	s_nop 0
	s_nop 0
	s_nop 0
	s_nop 0
	s_nop 0
	s_nop 0
	s_nop 0
	s_nop 0
	s_nop 0
	s_nop 0
	s_nop 0
	s_nop 0
	s_nop 0
	s_nop 0
	s_nop 0
	s_nop 0
	s_nop 0
	s_nop 0
	s_nop 0
	s_nop 0
	s_nop 0
	s_nop 0
	s_nop 0
	s_nop 0
	s_nop 0
	s_nop 0
	s_nop 0
	s_nop 0
	s_nop 0
	s_nop 0
	s_nop 0
	s_nop 0
	s_nop 0
	s_nop 0
	s_nop 0
	s_nop 0
	s_nop 0
	s_nop 0
	s_nop 0
	s_nop 0
	s_nop 0
	s_nop 0
	s_nop 0
	s_nop 0
	s_nop 0
	s_nop 0
	s_nop 0
	s_nop 0
	s_nop 0
	s_nop 0
	s_nop 0
	s_nop 0
	s_nop 0
	s_nop 0
	s_nop 0
	s_nop 0
	s_nop 0
	s_nop 0
	s_nop 0
	s_nop 0
	s_nop 0
	s_nop 0
	s_nop 0
	s_nop 0
	s_nop 0
	s_nop 0
	s_nop 0
	s_nop 0
	s_nop 0
	s_nop 0
	s_nop 0
	s_nop 0
	s_nop 0
	s_nop 0
	s_nop 0
	s_nop 0
	s_nop 0
	s_nop 0
	s_nop 0
	s_nop 0
	s_nop 0
	s_nop 0
	s_nop 0
	s_nop 0
	s_nop 0
	s_nop 0
	s_nop 0
	s_nop 0
	s_nop 0
	s_nop 0
	s_nop 0
	s_nop 0
	s_nop 0
	s_nop 0
	s_nop 0
	s_nop 0
	s_nop 0
	s_nop 0
	s_nop 0
	s_nop 0
	s_nop 0
	s_nop 0
	s_nop 0
	s_nop 0
	s_nop 0
	s_nop 0
	s_nop 0
	s_nop 0
	s_nop 0
	s_nop 0
	s_nop 0
	s_nop 0
	s_nop 0
	s_nop 0
	s_nop 0
	s_nop 0
	s_nop 0
	s_nop 0
	s_nop 0
	s_nop 0
	s_nop 0
	s_nop 0
	s_nop 0
	s_nop 0
	s_nop 0
	s_nop 0
	s_nop 0
	s_nop 0
	s_nop 0
	s_nop 0
	s_nop 0
	s_nop 0
	s_nop 0
	s_nop 0
	s_nop 0
	s_nop 0
	s_nop 0
	s_nop 0
	s_nop 0
	s_nop 0
	s_nop 0
	s_nop 0
	s_nop 0
	s_nop 0
	s_nop 0
	s_nop 0
	s_nop 0
	s_nop 0
	s_nop 0
	s_nop 0
	s_nop 0
	s_nop 0
	s_nop 0
	s_nop 0
	s_nop 0
	s_nop 0
	s_nop 0
	s_nop 0
	s_nop 0
	s_nop 0
	s_nop 0
	s_nop 0
	s_nop 0
	s_nop 0
	s_nop 0
	s_nop 0
	s_nop 0
	s_nop 0
	s_nop 0
	s_nop 0
	s_nop 0
	s_nop 0
	s_nop 0
	s_nop 0
	s_nop 0
	s_nop 0
	s_nop 0
	s_nop 0
	s_nop 0
	s_nop 0
	s_nop 0
	s_nop 0
	s_nop 0
	s_nop 0
	s_nop 0
	s_nop 0
	s_nop 0
	s_nop 0
	s_nop 0
	s_nop 0
	s_nop 0
	s_nop 0
	s_nop 0
	s_nop 0
	s_nop 0
	s_nop 0
	s_nop 0
	s_nop 0
	s_nop 0
	s_nop 0
	s_nop 0
	s_nop 0
	s_nop 0
	s_nop 0
	s_nop 0
	s_nop 0
	s_nop 0
	s_nop 0
	s_nop 0
	s_nop 0
	s_nop 0
	s_nop 0
	s_nop 0
	s_nop 0
	s_nop 0
	s_nop 0
	s_nop 0
	s_nop 0
	s_nop 0
	s_nop 0
	s_nop 0
	s_nop 0
	s_nop 0
	s_nop 0
	s_nop 0
	s_nop 0
	s_nop 0
	s_nop 0
	s_nop 0
	s_nop 0
	s_nop 0
	s_nop 0
	s_nop 0
	s_nop 0
	s_nop 0
	s_nop 0
	s_nop 0
	s_nop 0
	s_nop 0
	s_nop 0
	s_nop 0
	s_nop 0
	s_nop 0
	s_nop 0
	s_nop 0
	s_nop 0
	s_nop 0
	s_nop 0
	s_nop 0
	s_nop 0
	s_nop 0
	s_nop 0
	s_nop 0
	s_nop 0
	s_nop 0
	s_nop 0
	s_nop 0
	s_nop 0
	s_nop 0
	s_nop 0
	s_nop 0
	s_nop 0
	s_nop 0
	s_nop 0
	s_nop 0
	s_nop 0
	s_nop 0
	s_nop 0
	s_nop 0
	s_nop 0
	s_nop 0
	s_nop 0
	s_nop 0
	s_nop 0
	s_nop 0
	s_nop 0
	s_nop 0
	s_nop 0
	s_nop 0
	s_nop 0
	s_nop 0
	s_nop 0
	s_nop 0
	s_nop 0
	s_nop 0
	s_nop 0
	s_nop 0
	s_nop 0
	s_nop 0
	s_nop 0
	s_nop 0
	s_nop 0
	s_nop 0
	s_nop 0
	s_nop 0
	s_nop 0
	s_nop 0
	s_nop 0
	s_nop 0
	s_nop 0
	s_nop 0
	s_nop 0
	s_nop 0
	s_nop 0
	s_nop 0
	s_nop 0
	s_nop 0
	s_nop 0
	s_nop 0
	s_nop 0
	s_nop 0
	s_nop 0
	s_nop 0
	s_nop 0
	s_nop 0
	s_nop 0
	s_nop 0
	s_nop 0
	s_nop 0
	s_nop 0
	s_nop 0
	s_nop 0
	s_nop 0
	s_nop 0
	s_nop 0
	s_nop 0
	s_nop 0
	s_nop 0
	s_nop 0
	s_nop 0
	s_nop 0
	s_nop 0
	s_nop 0
	s_nop 0
	s_nop 0
	s_nop 0
	s_nop 0
	s_nop 0
	s_nop 0
	s_nop 0
	s_nop 0
	s_nop 0
	s_nop 0
	s_nop 0
	s_nop 0
	s_nop 0
	s_nop 0
	s_nop 0
	s_nop 0
	s_nop 0
	s_nop 0
	s_nop 0
	s_nop 0
	s_nop 0
	s_nop 0
	s_nop 0
	s_nop 0
	s_nop 0
	s_nop 0
	s_nop 0
	s_nop 0
	s_nop 0
	s_nop 0
	s_nop 0
	s_nop 0
	s_nop 0
	s_nop 0
	s_nop 0
	s_nop 0
	s_nop 0
	s_nop 0
	s_nop 0
	s_nop 0
	s_nop 0
	s_nop 0
	s_nop 0
	s_nop 0
	s_nop 0
	s_nop 0
	s_nop 0
	s_nop 0
	s_nop 0
	s_nop 0
	s_nop 0
	s_nop 0
	s_nop 0
	s_nop 0
	s_nop 0
	s_nop 0
	s_nop 0
	s_nop 0
	s_nop 0
	s_nop 0
	s_nop 0
	s_nop 0
	s_nop 0
	s_nop 0
	s_nop 0
	s_nop 0
	s_nop 0
	s_nop 0
	s_nop 0
	s_nop 0
	s_nop 0
	s_nop 0
	s_nop 0
	s_nop 0
	s_nop 0
	s_nop 0
	s_nop 0
	s_nop 0
	s_nop 0
	s_nop 0
	s_nop 0
	s_nop 0
	s_nop 0
	s_nop 0
	s_nop 0
	s_nop 0
	s_nop 0
	s_nop 0
	s_nop 0
	s_nop 0
	s_nop 0
	s_nop 0
	s_nop 0
	s_nop 0
	s_nop 0
	s_nop 0
	s_nop 0
	s_nop 0
	s_nop 0
	s_nop 0
	s_nop 0
	s_nop 0
	s_nop 0
	s_nop 0
	s_nop 0
	s_nop 0
	s_nop 0
	s_nop 0
	s_nop 0
	s_nop 0
	s_nop 0
	s_nop 0
	s_nop 0
	s_nop 0
	s_nop 0
	s_nop 0
	s_nop 0
	s_nop 0
	s_nop 0
	s_nop 0
	s_nop 0
	s_nop 0
	s_nop 0
	s_nop 0
	s_nop 0
	s_nop 0
	s_nop 0
	s_nop 0
	s_nop 0
	s_nop 0
	s_nop 0
	s_nop 0
	s_nop 0
	s_nop 0
	s_nop 0
	s_nop 0
	s_nop 0
	s_nop 0
	s_nop 0
	s_nop 0
	s_nop 0
	s_nop 0
	s_nop 0
	s_nop 0
	s_nop 0
	s_nop 0
	s_nop 0
	s_nop 0
	s_nop 0
	s_nop 0
	s_nop 0
	s_nop 0
	s_nop 0
	s_nop 0
	s_nop 0
	s_nop 0
	s_nop 0
	s_nop 0
	s_nop 0
	s_nop 0
	s_nop 0
	s_nop 0
	s_nop 0
	s_nop 0
	s_nop 0
	s_nop 0
	s_nop 0
	s_nop 0
	s_nop 0
	s_nop 0
	s_nop 0
	s_nop 0
	s_nop 0
	s_nop 0
	s_nop 0
	s_nop 0
	s_nop 0
	s_nop 0
	s_nop 0
	s_nop 0
	s_nop 0
	s_nop 0
	s_nop 0
	s_nop 0
	s_nop 0
	s_nop 0
	s_nop 0
	s_nop 0
	s_nop 0
	s_nop 0
	s_nop 0
	s_nop 0
	s_nop 0
	s_nop 0
	s_nop 0
	s_nop 0
	s_nop 0
	s_nop 0
	s_nop 0
	s_nop 0
	s_nop 0
	s_nop 0
	s_nop 0
	s_nop 0
	s_nop 0
	s_nop 0
	s_nop 0
	s_nop 0
	s_nop 0
	s_nop 0
	s_nop 0
	s_nop 0
	s_nop 0
	s_nop 0
	s_nop 0
	s_nop 0
; __device__ __forceinline__ CArgs cargs() { CArgs p = (CArgs)__builtin_amdgcn_kernarg_segment_ptr(); asm volatile("" : "+s"(p)); return p; }
; #define GRID_BAR_T(FIRST) do { XcdBarrier bb; bb.bar = (unsigned*)(cargs()->ws + WS_CTL) + CW_BAR; bb.x = xb_xcc_id(); bb.st = (volatile LAS unsigned*)(lds + MISC_OFF); \
;         xcd_barrier<FIRST>(bb, phase_tid(wv) == 0); } while (0)
; #define GRID_BAR_T(FIRST) do {} while (0)
; __global__ void __launch_bounds__(NTHR, 2) mk_fwd(Args a) {
;     ...
;     if (PM(0) && IN(0)) { phase_convert(cargs(), lds, wv); phase_convert_b(cargs(), lds, wv); }
;     if (IN(0) && IN(2)) GRID_BAR_T(true);
	s_nop 0
	s_nop 0
	s_nop 0
	s_nop 0
	s_nop 0
	s_nop 0
	s_nop 0
	s_nop 0
	s_nop 0
	s_nop 0
	s_nop 0
	s_nop 0
	s_nop 0
	s_nop 0
	s_nop 0
	s_nop 0
	s_nop 0
	s_nop 0
	s_nop 0
	s_nop 0
	s_nop 0
	s_nop 0
	s_nop 0
	s_nop 0
	s_nop 0
	s_nop 0
	s_nop 0
	s_nop 0
	s_nop 0
	s_nop 0
	s_nop 0
	s_nop 0
	s_nop 0
	s_nop 0
	s_nop 0
	s_nop 0
	s_nop 0
	s_nop 0
	s_nop 0
	s_nop 0
	s_nop 0
	s_nop 0
	s_nop 0
	s_nop 0
	s_nop 0
	s_nop 0
	s_nop 0
	s_nop 0
	s_nop 0
	s_nop 0
	s_nop 0
	s_nop 0
	s_nop 0
	s_nop 0
	s_nop 0
	s_nop 0
	s_nop 0
	s_nop 0
	s_nop 0
	s_nop 0
	s_nop 0
	s_nop 0
	s_nop 0
	s_nop 0
	s_nop 0
	s_nop 0
	s_nop 0
	s_nop 0
	s_nop 0
	s_nop 0
	s_nop 0
	s_nop 0
	s_nop 0
	s_nop 0
	s_nop 0
	s_nop 0
	s_nop 0
	s_nop 0
	s_nop 0
	s_nop 0
	s_nop 0
	s_nop 0
	s_nop 0
	s_nop 0
	s_nop 0
	s_nop 0
	s_nop 0
	s_nop 0
	s_nop 0
	s_nop 0
	s_nop 0
	s_nop 0
	s_nop 0
	s_nop 0
	s_nop 0
	s_nop 0
	s_nop 0
	s_nop 0
	s_nop 0
	s_nop 0
	s_nop 0
	s_nop 0
	s_nop 0
	s_nop 0
	s_nop 0
	s_nop 0
	s_nop 0
	s_nop 0
	s_nop 0
	s_nop 0
	s_nop 0
	s_nop 0
	s_nop 0
	s_nop 0
	s_nop 0
	s_nop 0
	s_nop 0
	s_nop 0
	s_nop 0
	s_nop 0
	s_nop 0
	s_nop 0
	s_nop 0
	s_nop 0
	s_nop 0
	s_nop 0
	s_nop 0
	s_nop 0
	s_nop 0
	s_nop 0
	s_nop 0
	s_nop 0
	s_nop 0
	s_nop 0
	s_nop 0
	s_nop 0
	s_nop 0
	s_nop 0
	s_nop 0
	s_nop 0
	s_nop 0
	s_nop 0
	s_nop 0
	s_nop 0
	s_nop 0
	s_nop 0
	s_nop 0
	s_nop 0
	s_nop 0
	s_nop 0
	s_nop 0
	s_nop 0
	s_nop 0
	s_nop 0
	s_nop 0
	s_nop 0
	s_nop 0
	s_nop 0
	s_nop 0
	s_nop 0
	s_nop 0
	s_nop 0
	s_nop 0
	s_nop 0
	s_nop 0
	s_nop 0
	s_nop 0
	s_nop 0
	s_nop 0
	s_nop 0
	s_nop 0
	s_nop 0
	s_nop 0
	s_nop 0
	s_nop 0
	s_nop 0
	s_nop 0
	s_nop 0
	s_nop 0
	s_nop 0
	s_nop 0
	s_nop 0
	s_nop 0
	s_nop 0
	s_nop 0
	s_nop 0
	s_nop 0
	s_nop 0
	s_nop 0
	s_nop 0
	s_nop 0
	s_nop 0
	s_nop 0
	s_nop 0
	s_nop 0
	s_nop 0
	s_nop 0
	s_nop 0
	s_nop 0
	s_nop 0
	s_nop 0
	s_nop 0
	s_nop 0
	s_nop 0
	s_nop 0
	s_nop 0
	s_nop 0
	s_nop 0
	s_nop 0
	s_nop 0
	s_nop 0
	s_nop 0
	s_nop 0
	s_nop 0
	s_nop 0
	s_nop 0
	s_nop 0
	s_nop 0
	s_nop 0
	s_nop 0
	s_nop 0
	s_nop 0
	s_nop 0
	s_nop 0
	s_nop 0
	s_nop 0
	s_nop 0
	s_nop 0
	s_nop 0
	s_nop 0
	s_nop 0
	s_nop 0
	s_nop 0
	s_nop 0
	s_nop 0
	s_nop 0
	s_nop 0
	s_nop 0
	s_nop 0
	s_nop 0
	s_nop 0
	s_nop 0
	s_nop 0
	s_nop 0
	s_nop 0
	s_nop 0
	s_nop 0
	s_nop 0
	s_nop 0
	s_nop 0
	s_nop 0
	s_nop 0
	s_nop 0
	s_nop 0
	s_nop 0
	s_nop 0
	s_nop 0
	s_nop 0
	s_nop 0
	s_nop 0
	s_nop 0
	s_nop 0
	s_nop 0
	s_nop 0
	s_nop 0
	s_nop 0
	s_nop 0
	s_nop 0
	s_nop 0
	s_nop 0
	s_nop 0
	s_nop 0
	s_nop 0
	s_nop 0
	s_nop 0
	s_nop 0
	s_nop 0
	s_nop 0
	s_nop 0
	s_nop 0
	s_nop 0
	s_nop 0
	s_nop 0
	s_nop 0
	s_nop 0
	s_nop 0
	s_nop 0
	s_nop 0
	s_nop 0
	s_nop 0
	s_nop 0
	s_nop 0
	s_nop 0
	s_nop 0
	s_nop 0
	s_nop 0
	s_nop 0
	s_nop 0
	s_nop 0
	s_nop 0
	s_nop 0
	s_nop 0
	s_nop 0
	s_nop 0
	s_nop 0
	s_nop 0
	s_nop 0
	s_nop 0
	s_nop 0
	s_nop 0
	s_nop 0
	s_nop 0
	s_nop 0
	s_nop 0
	s_nop 0
	s_nop 0
	s_nop 0
	s_nop 0
	s_nop 0
	s_nop 0
	s_nop 0
	s_nop 0
	s_nop 0
	s_nop 0
	s_nop 0
	s_nop 0
	s_nop 0
	s_nop 0
	s_nop 0
	s_nop 0
	s_nop 0
	s_nop 0
	s_nop 0
	s_nop 0
	s_nop 0
	s_nop 0
	s_nop 0
	s_nop 0
	s_nop 0
	s_nop 0
	s_nop 0
	s_nop 0
	s_nop 0
	s_nop 0
	s_nop 0
	s_nop 0
	s_nop 0
	s_nop 0
	s_nop 0
	s_nop 0
	s_nop 0
	s_nop 0
	s_nop 0
	s_nop 0
	s_nop 0
	s_nop 0
	s_nop 0
	s_nop 0
	s_nop 0
	s_nop 0
	s_nop 0
	s_nop 0
	s_nop 0
	s_nop 0
	s_nop 0
	s_nop 0
	s_nop 0
	s_nop 0
	s_nop 0
	s_nop 0
	s_nop 0
	s_nop 0
	s_nop 0
	s_nop 0
	s_nop 0
	s_nop 0
	s_nop 0
	s_nop 0
	s_nop 0
	s_nop 0
	s_nop 0
	s_nop 0
	s_nop 0
	s_nop 0
	s_nop 0
	s_nop 0
	s_nop 0
	s_nop 0
	s_nop 0
	s_nop 0
	s_nop 0
	s_nop 0
	s_nop 0
	s_nop 0
	s_nop 0
	s_nop 0
	s_nop 0
	s_nop 0
	s_nop 0
	s_nop 0
	s_nop 0
	s_nop 0
	s_nop 0
	s_nop 0
	s_nop 0
	s_nop 0
	s_nop 0
	s_nop 0
	s_nop 0
	s_nop 0
	s_nop 0
	s_nop 0
	s_nop 0
	s_nop 0
	s_nop 0
	s_nop 0
	s_nop 0
	s_nop 0
	s_nop 0
	s_nop 0
	s_nop 0
	s_nop 0
	s_nop 0
	s_nop 0
	s_nop 0
	s_nop 0
	s_nop 0
	s_nop 0
	s_nop 0
	s_nop 0
	s_nop 0
	s_nop 0
	s_nop 0
	s_nop 0
	s_nop 0
	s_nop 0
	s_nop 0
	s_nop 0
	s_nop 0
	s_nop 0
	s_nop 0
	s_nop 0
	s_nop 0
	s_nop 0
	s_nop 0
	s_nop 0
	s_nop 0
	s_nop 0
	s_nop 0
	s_nop 0
	s_nop 0
	s_nop 0
	s_nop 0
	s_nop 0
	s_nop 0
	s_nop 0
	s_nop 0
	s_nop 0
	s_nop 0
	s_nop 0
	s_nop 0
	s_nop 0
	s_nop 0
	s_nop 0
	s_nop 0
	s_nop 0
	s_nop 0
	s_nop 0
	s_nop 0
	s_nop 0
	s_nop 0
	s_nop 0
	s_nop 0
	s_nop 0
	s_nop 0
	s_nop 0
	s_nop 0
	s_nop 0
	s_nop 0
	s_nop 0
	s_nop 0
	s_nop 0
	s_nop 0
	s_nop 0
	s_nop 0
	s_nop 0
	s_nop 0
	s_nop 0
	s_nop 0
	s_nop 0
	s_nop 0
	s_nop 0
	s_nop 0
	s_nop 0
	s_nop 0
	s_nop 0
	s_nop 0
	s_nop 0
	s_nop 0
	s_nop 0
	s_nop 0
	s_nop 0
	s_nop 0
	s_nop 0
	s_nop 0
	s_nop 0
	s_nop 0
	s_nop 0
	s_nop 0
	s_nop 0
	s_nop 0
	s_nop 0
	s_nop 0
	s_nop 0
	s_nop 0
	s_nop 0
	s_nop 0
	s_nop 0
	s_nop 0
	s_nop 0
	s_nop 0
	s_nop 0
	s_nop 0
	s_nop 0
	s_nop 0
	s_nop 0
	s_nop 0
	s_nop 0
	s_nop 0
	s_nop 0
	s_nop 0
	s_nop 0
	s_nop 0
	s_nop 0
	s_nop 0
	s_nop 0
	s_nop 0
	s_nop 0
	s_nop 0
	s_nop 0
	s_nop 0
	s_nop 0
	s_nop 0
	s_nop 0
	s_nop 0
	s_nop 0
	s_nop 0
	s_nop 0
	s_nop 0
	s_nop 0
	s_nop 0
	s_nop 0
	s_nop 0
	s_nop 0
	s_nop 0
	s_nop 0
	s_nop 0
	s_nop 0
	s_nop 0
	s_nop 0
	s_nop 0
	s_nop 0
	s_nop 0
	s_nop 0
	s_nop 0
	s_nop 0
	s_nop 0
	s_nop 0
	s_nop 0
	s_nop 0
	s_nop 0
	s_nop 0
	s_nop 0
	s_nop 0
	s_nop 0
	s_nop 0
	s_nop 0
	s_nop 0
	s_nop 0
	s_nop 0
	s_nop 0
	s_nop 0
	s_nop 0
	s_nop 0
	s_nop 0
	s_nop 0
	s_nop 0
	s_nop 0
	s_nop 0
	s_nop 0
	s_nop 0
	s_nop 0
	s_nop 0
	s_nop 0
	s_nop 0
	s_nop 0
	s_nop 0
	s_nop 0
	s_nop 0
	s_nop 0
	s_nop 0
	s_nop 0
	s_nop 0
	s_nop 0
	s_nop 0
	s_nop 0
	s_nop 0
	s_nop 0
	s_nop 0
	s_nop 0
	s_nop 0
	s_nop 0
	s_nop 0
	s_nop 0
	s_nop 0
	s_nop 0
	s_nop 0
	s_nop 0
	s_nop 0
	s_nop 0
	s_nop 0
	s_nop 0
	s_nop 0
	s_nop 0
	s_nop 0
	s_nop 0
	s_nop 0
; __device__ __forceinline__ CArgs cargs() { CArgs p = (CArgs)__builtin_amdgcn_kernarg_segment_ptr(); asm volatile("" : "+s"(p)); return p; }
; #define GRID_BAR_T(FIRST) do { XcdBarrier bb; bb.bar = (unsigned*)(cargs()->ws + WS_CTL) + CW_BAR; bb.x = xb_xcc_id(); bb.st = (volatile LAS unsigned*)(lds + MISC_OFF); \
;         xcd_barrier<FIRST>(bb, phase_tid(wv) == 0); } while (0)
; #define GRID_BAR_T(FIRST) do {} while (0)
; __global__ void __launch_bounds__(NTHR, 2) mk_fwd(Args a) {
;     ...
;     if (PM(0) && IN(0)) { phase_convert(cargs(), lds, wv); phase_convert_b(cargs(), lds, wv); }
;     if (IN(0) && IN(2)) GRID_BAR_T(true);
	s_nop 0
	s_nop 0
	s_nop 0
	s_nop 0
	s_nop 0
	s_nop 0
	s_nop 0
	s_nop 0
	s_nop 0
	s_nop 0
	s_nop 0
	s_nop 0
	s_nop 0
	s_nop 0
	s_nop 0
	s_nop 0
	s_nop 0
	s_nop 0
	s_nop 0
	s_nop 0
	s_nop 0
	s_nop 0
	s_nop 0
	s_nop 0
	s_nop 0
	s_nop 0
	s_nop 0
	s_nop 0
	s_nop 0
	s_nop 0
	s_nop 0
	s_nop 0
	s_nop 0
	s_nop 0
	s_nop 0
	s_nop 0
	s_nop 0
	s_nop 0
	s_nop 0
	s_nop 0
	s_nop 0
	s_nop 0
	s_nop 0
	s_nop 0
	s_nop 0
	s_nop 0
	s_nop 0
	s_nop 0
	s_nop 0
	s_nop 0
	s_nop 0
	s_nop 0
	s_nop 0
	s_nop 0
	s_nop 0
	s_nop 0
	s_nop 0
	s_nop 0
	s_nop 0
	s_nop 0
	s_nop 0
	s_nop 0
	s_nop 0
	s_nop 0
	s_nop 0
	s_nop 0
	s_nop 0
	s_nop 0
	s_nop 0
	s_nop 0
	s_nop 0
	s_nop 0
	s_nop 0
	s_nop 0
	s_nop 0
	s_nop 0
	s_nop 0
	s_nop 0
	s_nop 0
	s_nop 0
	s_nop 0
	s_nop 0
	s_nop 0
	s_nop 0
	s_nop 0
	s_nop 0
	s_nop 0
	s_nop 0
	s_nop 0
	s_nop 0
	s_nop 0
	s_nop 0
	s_nop 0
	s_nop 0
	s_nop 0
	s_nop 0
	s_nop 0
	s_nop 0
	s_nop 0
	s_nop 0
	s_nop 0
	s_nop 0
	s_nop 0
	s_nop 0
	s_nop 0
	s_nop 0
	s_nop 0
	s_nop 0
	s_nop 0
	s_nop 0
	s_nop 0
	s_nop 0
	s_nop 0
	s_nop 0
	s_nop 0
	s_nop 0
	s_nop 0
	s_nop 0
	s_nop 0
	s_nop 0
	s_nop 0
	s_nop 0
	s_nop 0
	s_nop 0
	s_nop 0
	s_nop 0
	s_nop 0
	s_nop 0
	s_nop 0
	s_nop 0
	s_nop 0
	s_nop 0
	s_nop 0
	s_nop 0
	s_nop 0
	s_nop 0
	s_nop 0
	s_nop 0
	s_nop 0
	s_nop 0
	s_nop 0
	s_nop 0
	s_nop 0
	s_nop 0
	s_nop 0
	s_nop 0
	s_nop 0
	s_nop 0
	s_nop 0
	s_nop 0
	s_nop 0
	s_nop 0
	s_nop 0
	s_nop 0
	s_nop 0
	s_nop 0
	s_nop 0
	s_nop 0
	s_nop 0
	s_nop 0
	s_nop 0
	s_nop 0
	s_nop 0
	s_nop 0
	s_nop 0
	s_nop 0
	s_nop 0
	s_nop 0
	s_nop 0
	s_nop 0
	s_nop 0
	s_nop 0
	s_nop 0
	s_nop 0
	s_nop 0
	s_nop 0
	s_nop 0
	s_nop 0
	s_nop 0
	s_nop 0
	s_nop 0
	s_nop 0
	s_nop 0
	s_nop 0
	s_nop 0
	s_nop 0
	s_nop 0
	s_nop 0
	s_nop 0
	s_nop 0
	s_nop 0
	s_nop 0
	s_nop 0
	s_nop 0
	s_nop 0
	s_nop 0
	s_nop 0
	s_nop 0
	s_nop 0
	s_nop 0
	s_nop 0
	s_nop 0
	s_nop 0
	s_nop 0
	s_nop 0
	s_nop 0
	s_nop 0
	s_nop 0
	s_nop 0
	s_nop 0
	s_nop 0
	s_nop 0
	s_nop 0
	s_nop 0
	s_nop 0
	s_nop 0
	s_nop 0
	s_nop 0
	s_nop 0
	s_nop 0
	s_nop 0
	s_nop 0
	s_nop 0
	s_nop 0
	s_nop 0
	s_nop 0
	s_nop 0
	s_nop 0
	s_nop 0
	s_nop 0
	s_nop 0
	s_nop 0
	s_nop 0
	s_nop 0
	s_nop 0
	s_nop 0
	s_nop 0
	s_nop 0
	s_nop 0
	s_nop 0
	s_nop 0
	s_nop 0
	s_nop 0
	s_nop 0
	s_nop 0
	s_nop 0
	s_nop 0
	s_nop 0
	s_nop 0
	s_nop 0
	s_nop 0
	s_nop 0
	s_nop 0
	s_nop 0
	s_nop 0
	s_nop 0
	s_nop 0
	s_nop 0
	s_nop 0
	s_nop 0
	s_nop 0
	s_nop 0
	s_nop 0
	s_nop 0
	s_nop 0
	s_nop 0
	s_nop 0
	s_nop 0
	s_nop 0
	s_nop 0
	s_nop 0
	s_nop 0
	s_nop 0
	s_nop 0
	s_nop 0
	s_nop 0
	s_nop 0
	s_nop 0
	s_nop 0
	s_nop 0
	s_nop 0
	s_nop 0
	s_nop 0
	s_nop 0
	s_nop 0
	s_nop 0
	s_nop 0
	s_nop 0
	s_nop 0
	s_nop 0
	s_nop 0
	s_nop 0
	s_nop 0
	s_nop 0
	s_nop 0
	s_nop 0
	s_nop 0
	s_nop 0
	s_nop 0
	s_nop 0
	s_nop 0
	s_nop 0
	s_nop 0
	s_nop 0
	s_nop 0
	s_nop 0
	s_nop 0
	s_nop 0
	s_nop 0
	s_nop 0
	s_nop 0
	s_nop 0
	s_nop 0
	s_nop 0
	s_nop 0
	s_nop 0
	s_nop 0
	s_nop 0
	s_nop 0
	s_nop 0
	s_nop 0
	s_nop 0
	s_nop 0
	s_nop 0
	s_nop 0
	s_nop 0
	s_nop 0
	s_nop 0
	s_nop 0
	s_nop 0
	s_nop 0
	s_nop 0
	s_nop 0
	s_nop 0
	s_nop 0
	s_nop 0
	s_nop 0
	s_nop 0
	s_nop 0
	s_nop 0
	s_nop 0
	s_nop 0
	s_nop 0
	s_nop 0
	s_nop 0
	s_nop 0
	s_nop 0
	s_nop 0
	s_nop 0
	s_nop 0
	s_nop 0
	s_nop 0
	s_nop 0
	s_nop 0
	s_nop 0
	s_nop 0
	s_nop 0
	s_nop 0
	s_nop 0
	s_nop 0
	s_nop 0
	s_nop 0
	s_nop 0
	s_nop 0
	s_nop 0
	s_nop 0
	s_nop 0
	s_nop 0
	s_nop 0
	s_nop 0
	s_nop 0
	s_nop 0
	s_nop 0
	s_nop 0
	s_nop 0
	s_nop 0
	s_nop 0
	s_nop 0
	s_nop 0
	s_nop 0
	s_nop 0
	s_nop 0
	s_nop 0
	s_nop 0
	s_nop 0
	s_nop 0
	s_nop 0
	s_nop 0
	s_nop 0
	s_nop 0
	s_nop 0
	s_nop 0
	s_nop 0
	s_nop 0
	s_nop 0
	s_nop 0
	s_nop 0
	s_nop 0
	s_nop 0
	s_nop 0
	s_nop 0
	s_nop 0
	s_nop 0
	s_nop 0
	s_nop 0
	s_nop 0
	s_nop 0
	s_nop 0
	s_nop 0
	s_nop 0
	s_nop 0
	s_nop 0
	s_nop 0
	s_nop 0
	s_nop 0
	s_nop 0
	s_nop 0
	s_nop 0
	s_nop 0
	s_nop 0
	s_nop 0
	s_nop 0
	s_nop 0
	s_nop 0
	s_nop 0
	s_nop 0
	s_nop 0
	s_nop 0
	s_nop 0
	s_nop 0
	s_nop 0
	s_nop 0
	s_nop 0
	s_nop 0
	s_nop 0
	s_nop 0
	s_nop 0
	s_nop 0
	s_nop 0
	s_nop 0
	s_nop 0
	s_nop 0
	s_nop 0
	s_nop 0
	s_nop 0
	s_nop 0
	s_nop 0
	s_nop 0
	s_nop 0
	s_nop 0
	s_nop 0
	s_nop 0
	s_nop 0
	s_nop 0
	s_nop 0
	s_nop 0
	s_nop 0
	s_nop 0
	s_nop 0
	s_nop 0
	s_nop 0
	s_nop 0
	s_nop 0
	s_nop 0
	s_nop 0
	s_nop 0
	s_nop 0
	s_nop 0
	s_nop 0
	s_nop 0
	s_nop 0
	s_nop 0
	s_nop 0
	s_nop 0
	s_nop 0
	s_nop 0
	s_nop 0
	s_nop 0
	s_nop 0
	s_nop 0
	s_nop 0
	s_nop 0
	s_nop 0
	s_nop 0
	s_nop 0
	s_nop 0
	s_nop 0
	s_nop 0
	s_nop 0
	s_nop 0
	s_nop 0
	s_nop 0
	s_nop 0
	s_nop 0
	s_nop 0
	s_nop 0
	s_nop 0
	s_nop 0
	s_nop 0
	s_nop 0
	s_nop 0
	s_nop 0
	s_nop 0
	s_nop 0
	s_nop 0
	s_nop 0
	s_nop 0
	s_nop 0
	s_nop 0
	s_nop 0
	s_nop 0
	s_nop 0
	s_nop 0
	s_nop 0
	s_nop 0
	s_nop 0
	s_nop 0
	s_nop 0
	s_nop 0
	s_nop 0
	s_nop 0
	s_nop 0
	s_nop 0
	s_nop 0
	s_nop 0
	s_nop 0
	s_nop 0
	s_nop 0
	s_nop 0
	s_nop 0
	s_nop 0
	s_nop 0
	s_nop 0
	s_nop 0
	s_nop 0
	s_nop 0
	s_nop 0
	s_nop 0
	s_nop 0
	s_nop 0
	s_nop 0
	s_nop 0
	s_nop 0
	s_nop 0
	s_nop 0
	s_nop 0
	s_nop 0
	s_nop 0
	s_nop 0
	s_nop 0
	s_nop 0
	s_nop 0
	s_nop 0
	s_nop 0
	s_nop 0
	s_nop 0
	s_nop 0
	s_nop 0
	s_nop 0
	s_nop 0
	s_nop 0
	s_nop 0
	s_nop 0
	s_nop 0
	s_nop 0
	s_nop 0
	s_nop 0
	s_nop 0
	s_nop 0
	s_nop 0
	s_nop 0
	s_nop 0
	s_nop 0
	s_nop 0
	s_nop 0
	s_nop 0
	s_nop 0
	s_nop 0
	s_nop 0
	s_nop 0
	s_nop 0
	s_nop 0
	s_nop 0
	s_nop 0
	s_nop 0
	s_nop 0
	s_nop 0
	s_nop 0
	s_nop 0
	s_nop 0
	s_nop 0
	s_nop 0
	s_nop 0
	s_nop 0
	s_nop 0
	s_nop 0
	s_nop 0
	s_nop 0
	s_nop 0
	s_nop 0
	s_nop 0
	s_nop 0
	s_nop 0
	s_nop 0
	s_nop 0
	s_nop 0
	s_nop 0
	s_nop 0
	s_nop 0
	s_nop 0
	s_nop 0
	s_nop 0
	s_nop 0
	s_nop 0
	s_nop 0
	s_nop 0
	s_nop 0
	s_nop 0
	s_nop 0
	s_nop 0
	s_nop 0
	s_nop 0
	s_nop 0
	s_nop 0
	s_nop 0
	s_nop 0
	s_nop 0
; __device__ __forceinline__ CArgs cargs() { CArgs p = (CArgs)__builtin_amdgcn_kernarg_segment_ptr(); asm volatile("" : "+s"(p)); return p; }
; #define GRID_BAR_T(FIRST) do { XcdBarrier bb; bb.bar = (unsigned*)(cargs()->ws + WS_CTL) + CW_BAR; bb.x = xb_xcc_id(); bb.st = (volatile LAS unsigned*)(lds + MISC_OFF); \
;         xcd_barrier<FIRST>(bb, phase_tid(wv) == 0); } while (0)
; #define GRID_BAR_T(FIRST) do {} while (0)
; __global__ void __launch_bounds__(NTHR, 2) mk_fwd(Args a) {
;     ...
;     if (PM(0) && IN(0)) { phase_convert(cargs(), lds, wv); phase_convert_b(cargs(), lds, wv); }
;     if (IN(0) && IN(2)) GRID_BAR_T(true);
	s_nop 0
	s_nop 0
	s_nop 0
	s_nop 0
	s_nop 0
	s_nop 0
	s_nop 0
	s_nop 0
	s_nop 0
	s_nop 0
	s_nop 0
	s_nop 0
	s_nop 0
	s_nop 0
	s_nop 0
	s_nop 0
	s_nop 0
	s_nop 0
	s_nop 0
	s_nop 0
	s_nop 0
	s_nop 0
	s_nop 0
	s_nop 0
	s_nop 0
	s_nop 0
	s_nop 0
	s_nop 0
	s_nop 0
	s_nop 0
	s_nop 0
	s_nop 0
	s_nop 0
	s_nop 0
	s_nop 0
	s_nop 0
	s_nop 0
	s_nop 0
	s_nop 0
	s_nop 0
	s_nop 0
	s_nop 0
	s_nop 0
	s_nop 0
	s_nop 0
	s_nop 0
	s_nop 0
	s_nop 0
	s_nop 0
	s_nop 0
	s_nop 0
	s_nop 0
	s_nop 0
	s_nop 0
	s_nop 0
	s_nop 0
	s_nop 0
	s_nop 0
	s_nop 0
	s_nop 0
	s_nop 0
	s_nop 0
	s_nop 0
	s_nop 0
	s_nop 0
	s_nop 0
	s_nop 0
	s_nop 0
	s_nop 0
	s_nop 0
	s_nop 0
	s_nop 0
	s_nop 0
	s_nop 0
	s_nop 0
	s_nop 0
	s_nop 0
	s_nop 0
	s_nop 0
	s_nop 0
	s_nop 0
	s_nop 0
	s_nop 0
	s_nop 0
	s_nop 0
	s_nop 0
	s_nop 0
	s_nop 0
	s_nop 0
	s_nop 0
	s_nop 0
	s_nop 0
	s_nop 0
	s_nop 0
	s_nop 0
	s_nop 0
	s_nop 0
	s_nop 0
	s_nop 0
	s_nop 0
	s_nop 0
	s_nop 0
	s_nop 0
	s_nop 0
	s_nop 0
	s_nop 0
	s_nop 0
	s_nop 0
	s_nop 0
	s_nop 0
	s_nop 0
	s_nop 0
	s_nop 0
	s_nop 0
	s_nop 0
	s_nop 0
	s_nop 0
	s_nop 0
	s_nop 0
	s_nop 0
	s_nop 0
	s_nop 0
	s_nop 0
	s_nop 0
	s_nop 0
	s_nop 0
	s_nop 0
	s_nop 0
	s_nop 0
	s_nop 0
	s_nop 0
	s_nop 0
	s_nop 0
	s_nop 0
	s_nop 0
	s_nop 0
	s_nop 0
	s_nop 0
	s_nop 0
	s_nop 0
	s_nop 0
	s_nop 0
	s_nop 0
	s_nop 0
	s_nop 0
	s_nop 0
	s_nop 0
	s_nop 0
	s_nop 0
	s_nop 0
	s_nop 0
	s_nop 0
	s_nop 0
	s_nop 0
	s_nop 0
	s_nop 0
	s_nop 0
	s_nop 0
	s_nop 0
	s_nop 0
	s_nop 0
	s_nop 0
	s_nop 0
	s_nop 0
	s_nop 0
	s_nop 0
	s_nop 0
	s_nop 0
	s_nop 0
	s_nop 0
	s_nop 0
	s_nop 0
	s_nop 0
	s_nop 0
	s_nop 0
	s_nop 0
	s_nop 0
	s_nop 0
	s_nop 0
	s_nop 0
	s_nop 0
	s_nop 0
	s_nop 0
	s_nop 0
	s_nop 0
	s_nop 0
	s_nop 0
	s_nop 0
	s_nop 0
	s_nop 0
	s_nop 0
	s_nop 0
	s_nop 0
	s_nop 0
	s_nop 0
	s_nop 0
	s_nop 0
	s_nop 0
	s_nop 0
	s_nop 0
	s_nop 0
	s_nop 0
	s_nop 0
	s_nop 0
	s_nop 0
	s_nop 0
	s_nop 0
	s_nop 0
	s_nop 0
	s_nop 0
	s_nop 0
	s_nop 0
	s_nop 0
	s_nop 0
	s_nop 0
	s_nop 0
	s_nop 0
	s_nop 0
	s_nop 0
	s_nop 0
	s_nop 0
	s_nop 0
	s_nop 0
	s_nop 0
	s_nop 0
	s_nop 0
	s_nop 0
	s_nop 0
	s_nop 0
	s_nop 0
	s_nop 0
	s_nop 0
	s_nop 0
	s_nop 0
	s_nop 0
	s_nop 0
	s_nop 0
	s_nop 0
	s_nop 0
	s_nop 0
	s_nop 0
	s_nop 0
	s_nop 0
	s_nop 0
	s_nop 0
	s_nop 0
	s_nop 0
	s_nop 0
	s_nop 0
	s_nop 0
	s_nop 0
	s_nop 0
	s_nop 0
	s_nop 0
	s_nop 0
	s_nop 0
	s_nop 0
	s_nop 0
	s_nop 0
	s_nop 0
	s_nop 0
	s_nop 0
	s_nop 0
	s_nop 0
	s_nop 0
	s_nop 0
	s_nop 0
	s_nop 0
	s_nop 0
	s_nop 0
	s_nop 0
	s_nop 0
	s_nop 0
	s_nop 0
	s_nop 0
	s_nop 0
	s_nop 0
	s_nop 0
	s_nop 0
	s_nop 0
	s_nop 0
	s_nop 0
	s_nop 0
	s_nop 0
	s_nop 0
	s_nop 0
	s_nop 0
	s_nop 0
	s_nop 0
	s_nop 0
	s_nop 0
	s_nop 0
	s_nop 0
	s_nop 0
	s_nop 0
	s_nop 0
	s_nop 0
	s_nop 0
	s_nop 0
	s_nop 0
	s_nop 0
	s_nop 0
	s_nop 0
	s_nop 0
	s_nop 0
	s_nop 0
	s_nop 0
	s_nop 0
	s_nop 0
	s_nop 0
	s_nop 0
	s_nop 0
	s_nop 0
	s_nop 0
	s_nop 0
	s_nop 0
	s_nop 0
	s_nop 0
	s_nop 0
	s_nop 0
	s_nop 0
	s_nop 0
	s_nop 0
	s_nop 0
	s_nop 0
	s_nop 0
	s_nop 0
	s_nop 0
	s_nop 0
	s_nop 0
	s_nop 0
	s_nop 0
	s_nop 0
	s_nop 0
	s_nop 0
	s_nop 0
	s_nop 0
	s_nop 0
	s_nop 0
	s_nop 0
	s_nop 0
	s_nop 0
	s_nop 0
	s_nop 0
	s_nop 0
	s_nop 0
	s_nop 0
	s_nop 0
	s_nop 0
	s_nop 0
	s_nop 0
	s_nop 0
	s_nop 0
	s_nop 0
	s_nop 0
	s_nop 0
	s_nop 0
	s_nop 0
	s_nop 0
	s_nop 0
	s_nop 0
	s_nop 0
	s_nop 0
	s_nop 0
	s_nop 0
	s_nop 0
	s_nop 0
	s_nop 0
	s_nop 0
	s_nop 0
	s_nop 0
	s_nop 0
	s_nop 0
	s_nop 0
	s_nop 0
	s_nop 0
	s_nop 0
	s_nop 0
	s_nop 0
	s_nop 0
	s_nop 0
	s_nop 0
	s_nop 0
	s_nop 0
	s_nop 0
	s_nop 0
	s_nop 0
	s_nop 0
	s_nop 0
	s_nop 0
	s_nop 0
	s_nop 0
	s_nop 0
	s_nop 0
	s_nop 0
	s_nop 0
	s_nop 0
	s_nop 0
	s_nop 0
	s_nop 0
	s_nop 0
	s_nop 0
	s_nop 0
	s_nop 0
	s_nop 0
	s_nop 0
	s_nop 0
	s_nop 0
	s_nop 0
	s_nop 0
	s_nop 0
	s_nop 0
	s_nop 0
	s_nop 0
	s_nop 0
	s_nop 0
	s_nop 0
	s_nop 0
	s_nop 0
	s_nop 0
	s_nop 0
	s_nop 0
	s_nop 0
	s_nop 0
	s_nop 0
	s_nop 0
	s_nop 0
	s_nop 0
	s_nop 0
	s_nop 0
	s_nop 0
	s_nop 0
	s_nop 0
	s_nop 0
	s_nop 0
	s_nop 0
	s_nop 0
	s_nop 0
	s_nop 0
	s_nop 0
	s_nop 0
	s_nop 0
	s_nop 0
	s_nop 0
	s_nop 0
	s_nop 0
	s_nop 0
	s_nop 0
	s_nop 0
	s_nop 0
	s_nop 0
	s_nop 0
	s_nop 0
	s_nop 0
	s_nop 0
	s_nop 0
	s_nop 0
	s_nop 0
	s_nop 0
	s_nop 0
	s_nop 0
	s_nop 0
	s_nop 0
	s_nop 0
	s_nop 0
	s_nop 0
	s_nop 0
	s_nop 0
	s_nop 0
	s_nop 0
	s_nop 0
	s_nop 0
	s_nop 0
	s_nop 0
	s_nop 0
	s_nop 0
	s_nop 0
	s_nop 0
	s_nop 0
	s_nop 0
	s_nop 0
	s_nop 0
	s_nop 0
	s_nop 0
	s_nop 0
	s_nop 0
	s_nop 0
	s_nop 0
	s_nop 0
	s_nop 0
	s_nop 0
	s_nop 0
	s_nop 0
	s_nop 0
	s_nop 0
	s_nop 0
	s_nop 0
	s_nop 0
	s_nop 0
	s_nop 0
	s_nop 0
	s_nop 0
	s_nop 0
	s_nop 0
	s_nop 0
	s_nop 0
	s_nop 0
	s_nop 0
	s_nop 0
	s_nop 0
	s_nop 0
	s_nop 0
	s_nop 0
	s_nop 0
	s_nop 0
	s_nop 0
	s_nop 0
	s_nop 0
	s_nop 0
	s_nop 0
	s_nop 0
	s_nop 0
	s_nop 0
	s_nop 0
	s_nop 0
	s_nop 0
	s_nop 0
	s_nop 0
	s_nop 0
	s_nop 0
	s_nop 0
	s_nop 0
	s_nop 0
	s_nop 0
	s_nop 0
	s_nop 0
	s_nop 0
	s_nop 0
	s_nop 0
	s_nop 0
	s_nop 0
	s_nop 0
	s_nop 0
	s_nop 0
	s_nop 0
	s_nop 0
	s_nop 0
	s_nop 0
	s_nop 0
	s_nop 0
	s_nop 0
	s_nop 0
	s_nop 0
	s_nop 0
	s_nop 0
	s_nop 0
	s_nop 0
	s_nop 0
	s_nop 0
	s_nop 0
	s_nop 0
	s_nop 0
	s_nop 0
	s_nop 0
	s_nop 0
	s_nop 0
	s_nop 0
	s_nop 0
	s_nop 0
	s_nop 0
	s_nop 0
	s_nop 0
	s_nop 0
	s_nop 0
	s_nop 0
	s_nop 0
	s_nop 0
	s_nop 0
	s_nop 0
	s_nop 0
	s_nop 0
	s_nop 0
	s_nop 0
	s_nop 0
	s_nop 0
	s_nop 0
	s_nop 0
	s_nop 0
	s_nop 0
	s_nop 0
	s_nop 0
	s_nop 0
	s_nop 0
	s_nop 0
	s_nop 0
	s_nop 0
	s_nop 0
	s_nop 0
	s_nop 0
	s_nop 0
	s_nop 0
	s_nop 0
	s_nop 0
	s_nop 0
	s_nop 0
	s_nop 0
	s_nop 0
	s_nop 0
	s_nop 0
	s_nop 0
	s_nop 0
	s_nop 0
	s_nop 0
	s_nop 0
	s_nop 0
	s_nop 0
	s_nop 0
	s_nop 0
	s_nop 0
	s_nop 0
	s_nop 0
	s_nop 0
	s_nop 0
	s_nop 0
	s_nop 0
	s_nop 0
	s_nop 0
; __device__ __forceinline__ CArgs cargs() { CArgs p = (CArgs)__builtin_amdgcn_kernarg_segment_ptr(); asm volatile("" : "+s"(p)); return p; }
; #define GRID_BAR_T(FIRST) do { XcdBarrier bb; bb.bar = (unsigned*)(cargs()->ws + WS_CTL) + CW_BAR; bb.x = xb_xcc_id(); bb.st = (volatile LAS unsigned*)(lds + MISC_OFF); \
;         xcd_barrier<FIRST>(bb, phase_tid(wv) == 0); } while (0)
; #define GRID_BAR_T(FIRST) do {} while (0)
; __global__ void __launch_bounds__(NTHR, 2) mk_fwd(Args a) {
;     ...
;     if (PM(0) && IN(0)) { phase_convert(cargs(), lds, wv); phase_convert_b(cargs(), lds, wv); }
;     if (IN(0) && IN(2)) GRID_BAR_T(true);
	s_nop 0
	s_nop 0
	s_nop 0
	s_nop 0
	s_nop 0
	s_nop 0
	s_nop 0
	s_nop 0
	s_nop 0
	s_nop 0
	s_nop 0
	s_nop 0
	s_nop 0
	s_nop 0
	s_nop 0
	s_nop 0
	s_nop 0
	s_nop 0
	s_nop 0
	s_nop 0
	s_nop 0
	s_nop 0
	s_nop 0
	s_nop 0
	s_nop 0
	s_nop 0
	s_nop 0
	s_nop 0
	s_nop 0
	s_nop 0
	s_nop 0
	s_nop 0
	s_nop 0
	s_nop 0
	s_nop 0
	s_nop 0
	s_nop 0
	s_nop 0
	s_nop 0
	s_nop 0
	s_nop 0
	s_nop 0
	s_nop 0
	s_nop 0
	s_nop 0
	s_nop 0
	s_nop 0
	s_nop 0
	s_nop 0
	s_nop 0
	s_nop 0
	s_nop 0
	s_nop 0
	s_nop 0
	s_nop 0
	s_nop 0
	s_nop 0
	s_nop 0
	s_nop 0
	s_nop 0
	s_nop 0
	s_nop 0
	s_nop 0
	s_nop 0
	s_nop 0
	s_nop 0
	s_nop 0
	s_nop 0
	s_nop 0
	s_nop 0
	s_nop 0
	s_nop 0
	s_nop 0
	s_nop 0
	s_nop 0
	s_nop 0
	s_nop 0
	s_nop 0
	s_nop 0
	s_nop 0
	s_nop 0
	s_nop 0
	s_nop 0
	s_nop 0
	s_nop 0
	s_nop 0
	s_nop 0
	s_nop 0
	s_nop 0
	s_nop 0
	s_nop 0
	s_nop 0
	s_nop 0
	s_nop 0
	s_nop 0
	s_nop 0
	s_nop 0
	s_nop 0
	s_nop 0
	s_nop 0
	s_nop 0
	s_nop 0
	s_nop 0
	s_nop 0
	s_nop 0
	s_nop 0
	s_nop 0
	s_nop 0
	s_nop 0
	s_nop 0
	s_nop 0
	s_nop 0
	s_nop 0
	s_nop 0
	s_nop 0
	s_nop 0
	s_nop 0
	s_nop 0
	s_nop 0
	s_nop 0
	s_nop 0
	s_nop 0
	s_nop 0
	s_nop 0
	s_nop 0
	s_nop 0
	s_nop 0
	s_nop 0
	s_nop 0
	s_nop 0
	s_nop 0
	s_nop 0
	s_nop 0
	s_nop 0
	s_nop 0
	s_nop 0
	s_nop 0
	s_nop 0
	s_nop 0
	s_nop 0
	s_nop 0
	s_nop 0
	s_nop 0
	s_nop 0
	s_nop 0
	s_nop 0
	s_nop 0
	s_nop 0
	s_nop 0
	s_nop 0
	s_nop 0
	s_nop 0
	s_nop 0
	s_nop 0
	s_nop 0
	s_nop 0
	s_nop 0
	s_nop 0
	s_nop 0
	s_nop 0
	s_nop 0
	s_nop 0
	s_nop 0
	s_nop 0
	s_nop 0
	s_nop 0
	s_nop 0
	s_nop 0
	s_nop 0
	s_nop 0
	s_nop 0
	s_nop 0
	s_nop 0
	s_nop 0
	s_nop 0
	s_nop 0
	s_nop 0
	s_nop 0
	s_nop 0
	s_nop 0
	s_nop 0
	s_nop 0
	s_nop 0
	s_nop 0
	s_nop 0
	s_nop 0
	s_nop 0
	s_nop 0
	s_nop 0
	s_nop 0
	s_nop 0
	s_nop 0
	s_nop 0
	s_nop 0
	s_nop 0
	s_nop 0
	s_nop 0
	s_nop 0
	s_nop 0
	s_nop 0
	s_nop 0
	s_nop 0
	s_nop 0
	s_nop 0
	s_nop 0
	s_nop 0
	s_nop 0
	s_nop 0
	s_nop 0
	s_nop 0
	s_nop 0
	s_nop 0
	s_nop 0
	s_nop 0
	s_nop 0
	s_nop 0
	s_nop 0
	s_nop 0
	s_nop 0
	s_nop 0
	s_nop 0
	s_nop 0
	s_nop 0
	s_nop 0
	s_nop 0
	s_nop 0
	s_nop 0
	s_nop 0
	s_nop 0
	s_nop 0
	s_nop 0
	s_nop 0
	s_nop 0
	s_nop 0
	s_nop 0
	s_nop 0
	s_nop 0
	s_nop 0
	s_nop 0
	s_nop 0
	s_nop 0
	s_nop 0
	s_nop 0
	s_nop 0
	s_nop 0
	s_nop 0
	s_nop 0
	s_nop 0
	s_nop 0
	s_nop 0
	s_nop 0
	s_nop 0
	s_nop 0
	s_nop 0
	s_nop 0
	s_nop 0
	s_nop 0
	s_nop 0
	s_nop 0
	s_nop 0
	s_nop 0
	s_nop 0
	s_nop 0
	s_nop 0
	s_nop 0
	s_nop 0
	s_nop 0
	s_nop 0
	s_nop 0
	s_nop 0
	s_nop 0
	s_nop 0
	s_nop 0
	s_nop 0
	s_nop 0
	s_nop 0
	s_nop 0
	s_nop 0
	s_nop 0
	s_nop 0
	s_nop 0
	s_nop 0
	s_nop 0
	s_nop 0
	s_nop 0
	s_nop 0
	s_nop 0
	s_nop 0
	s_nop 0
	s_nop 0
	s_nop 0
	s_nop 0
	s_nop 0
	s_nop 0
	s_nop 0
	s_nop 0
	s_nop 0
	s_nop 0
	s_nop 0
	s_nop 0
	s_nop 0
	s_nop 0
	s_nop 0
	s_nop 0
	s_nop 0
	s_nop 0
	s_nop 0
	s_nop 0
	s_nop 0
	s_nop 0
	s_nop 0
	s_nop 0
	s_nop 0
	s_nop 0
	s_nop 0
	s_nop 0
	s_nop 0
	s_nop 0
	s_nop 0
	s_nop 0
	s_nop 0
	s_nop 0
	s_nop 0
	s_nop 0
	s_nop 0
	s_nop 0
	s_nop 0
	s_nop 0
	s_nop 0
	s_nop 0
	s_nop 0
	s_nop 0
	s_nop 0
	s_nop 0
	s_nop 0
	s_nop 0
	s_nop 0
	s_nop 0
	s_nop 0
	s_nop 0
	s_nop 0
	s_nop 0
	s_nop 0
	s_nop 0
	s_nop 0
	s_nop 0
	s_nop 0
	s_nop 0
	s_nop 0
	s_nop 0
	s_nop 0
	s_nop 0
	s_nop 0
	s_nop 0
	s_nop 0
	s_nop 0
	s_nop 0
	s_nop 0
	s_nop 0
	s_nop 0
	s_nop 0
	s_nop 0
	s_nop 0
	s_nop 0
	s_nop 0
	s_nop 0
	s_nop 0
	s_nop 0
	s_nop 0
	s_nop 0
	s_nop 0
	s_nop 0
	s_nop 0
	s_nop 0
	s_nop 0
	s_nop 0
	s_nop 0
	s_nop 0
	s_nop 0
	s_nop 0
	s_nop 0
	s_nop 0
	s_nop 0
	s_nop 0
	s_nop 0
	s_nop 0
	s_nop 0
	s_nop 0
	s_nop 0
	s_nop 0
	s_nop 0
	s_nop 0
	s_nop 0
	s_nop 0
	s_nop 0
	s_nop 0
	s_nop 0
	s_nop 0
	s_nop 0
	s_nop 0
	s_nop 0
	s_nop 0
	s_nop 0
	s_nop 0
	s_nop 0
	s_nop 0
	s_nop 0
	s_nop 0
	s_nop 0
	s_nop 0
	s_nop 0
	s_nop 0
	s_nop 0
	s_nop 0
	s_nop 0
	s_nop 0
	s_nop 0
	s_nop 0
	s_nop 0
	s_nop 0
	s_nop 0
	s_nop 0
	s_nop 0
	s_nop 0
	s_nop 0
	s_nop 0
	s_nop 0
	s_nop 0
	s_nop 0
	s_nop 0
	s_nop 0
	s_nop 0
	s_nop 0
	s_nop 0
	s_nop 0
	s_nop 0
	s_nop 0
	s_nop 0
	s_nop 0
	s_nop 0
	s_nop 0
	s_nop 0
	s_nop 0
	s_nop 0
	s_nop 0
	s_nop 0
	s_nop 0
	s_nop 0
	s_nop 0
	s_nop 0
	s_nop 0
	s_nop 0
	s_nop 0
	s_nop 0
	s_nop 0
	s_nop 0
	s_nop 0
	s_nop 0
	s_nop 0
	s_nop 0
	s_nop 0
	s_nop 0
	s_nop 0
	s_nop 0
	s_nop 0
	s_nop 0
	s_nop 0
	s_nop 0
	s_nop 0
	s_nop 0
	s_nop 0
	s_nop 0
	s_nop 0
	s_nop 0
	s_nop 0
	s_nop 0
	s_nop 0
	s_nop 0
	s_nop 0
	s_nop 0
	s_nop 0
	s_nop 0
	s_nop 0
	s_nop 0
	s_nop 0
	s_nop 0
	s_nop 0
	s_nop 0
	s_nop 0
	s_nop 0
	s_nop 0
	s_nop 0
	s_nop 0
	s_nop 0
	s_nop 0
	s_nop 0
	s_nop 0
	s_nop 0
	s_nop 0
	s_nop 0
	s_nop 0
	s_nop 0
	s_nop 0
	s_nop 0
	s_nop 0
	s_nop 0
	s_nop 0
	s_nop 0
	s_nop 0
	s_nop 0
	s_nop 0
	s_nop 0
	s_nop 0
	s_nop 0
	s_nop 0
	s_nop 0
	s_nop 0
	s_nop 0
	s_nop 0
	s_nop 0
	s_nop 0
	s_nop 0
	s_nop 0
	s_nop 0
	s_nop 0
	s_nop 0
	s_nop 0
	s_nop 0
	s_nop 0
	s_nop 0
	s_nop 0
	s_nop 0
	s_nop 0
	s_nop 0
	s_nop 0
	s_nop 0
	s_nop 0
	s_nop 0
	s_nop 0
	s_nop 0
	s_nop 0
	s_nop 0
	s_nop 0
	s_nop 0
	s_nop 0
	s_nop 0
	s_nop 0
	s_nop 0
	s_nop 0
	s_nop 0
	s_nop 0
	s_nop 0
	s_nop 0
	s_nop 0
	s_nop 0
	s_nop 0
	s_nop 0
	s_nop 0
	s_nop 0
	s_nop 0
	s_nop 0
	s_nop 0
	s_nop 0
	s_nop 0
	s_nop 0
	s_nop 0
	s_nop 0
	s_nop 0
	s_nop 0
	s_nop 0
	s_nop 0
	s_nop 0
	s_nop 0
	s_nop 0
	s_nop 0
	s_nop 0
	s_nop 0
	s_nop 0
	s_nop 0
	s_nop 0
	s_nop 0
	s_nop 0
	s_nop 0
	s_nop 0
	s_nop 0
	s_nop 0
	s_nop 0
	s_nop 0
	s_nop 0
	s_nop 0
	s_nop 0
	s_nop 0
	s_nop 0
	s_nop 0
	s_nop 0
	s_nop 0
	s_nop 0
	s_nop 0
	s_nop 0
	s_nop 0
	s_nop 0
	s_nop 0
	s_nop 0
	s_nop 0
	s_nop 0
	s_nop 0
	s_nop 0
	s_nop 0
	s_nop 0
	s_nop 0
	s_nop 0
	s_nop 0
	s_nop 0
	s_nop 0
	s_nop 0
	s_nop 0
	s_nop 0
	s_nop 0
	s_nop 0
	s_nop 0
	s_nop 0
	s_nop 0
	s_nop 0
	s_nop 0
	s_nop 0
	s_nop 0
	s_nop 0
; __device__ __forceinline__ CArgs cargs() { CArgs p = (CArgs)__builtin_amdgcn_kernarg_segment_ptr(); asm volatile("" : "+s"(p)); return p; }
; #define GRID_BAR_T(FIRST) do { XcdBarrier bb; bb.bar = (unsigned*)(cargs()->ws + WS_CTL) + CW_BAR; bb.x = xb_xcc_id(); bb.st = (volatile LAS unsigned*)(lds + MISC_OFF); \
;         xcd_barrier<FIRST>(bb, phase_tid(wv) == 0); } while (0)
; #define GRID_BAR_T(FIRST) do {} while (0)
; __global__ void __launch_bounds__(NTHR, 2) mk_fwd(Args a) {
;     ...
;     if (PM(0) && IN(0)) { phase_convert(cargs(), lds, wv); phase_convert_b(cargs(), lds, wv); }
;     if (IN(0) && IN(2)) GRID_BAR_T(true);
	s_nop 0
	s_nop 0
	s_nop 0
	s_nop 0
	s_nop 0
	s_nop 0
	s_nop 0
	s_nop 0
	s_nop 0
	s_nop 0
	s_nop 0
	s_nop 0
	s_nop 0
	s_nop 0
	s_nop 0
	s_nop 0
	s_nop 0
	s_nop 0
	s_nop 0
	s_nop 0
	s_nop 0
	s_nop 0
	s_nop 0
	s_nop 0
	s_nop 0
	s_nop 0
	s_nop 0
	s_nop 0
	s_nop 0
	s_nop 0
	s_nop 0
	s_nop 0
	s_nop 0
	s_nop 0
	s_nop 0
	s_nop 0
	s_nop 0
	s_nop 0
	s_nop 0
	s_nop 0
	s_nop 0
	s_nop 0
	s_nop 0
	s_nop 0
	s_nop 0
	s_nop 0
	s_nop 0
	s_nop 0
	s_nop 0
	s_nop 0
	s_nop 0
	s_nop 0
	s_nop 0
	s_nop 0
	s_nop 0
	s_nop 0
	s_nop 0
	s_nop 0
	s_nop 0
	s_nop 0
	s_nop 0
	s_nop 0
	s_nop 0
	s_nop 0
	s_nop 0
	s_nop 0
	s_nop 0
	s_nop 0
	s_nop 0
	s_nop 0
	s_nop 0
	s_nop 0
	s_nop 0
	s_nop 0
	s_nop 0
	s_nop 0
	s_nop 0
	s_nop 0
	s_nop 0
	s_nop 0
	s_nop 0
	s_nop 0
	s_nop 0
	s_nop 0
	s_nop 0
	s_nop 0
	s_nop 0
	s_nop 0
	s_nop 0
	s_nop 0
	s_nop 0
	s_nop 0
	s_nop 0
	s_nop 0
	s_nop 0
	s_nop 0
	s_nop 0
	s_nop 0
	s_nop 0
	s_nop 0
	s_nop 0
	s_nop 0
	s_nop 0
	s_nop 0
	s_nop 0
	s_nop 0
	s_nop 0
	s_nop 0
	s_nop 0
	s_nop 0
	s_nop 0
	s_nop 0
	s_nop 0
	s_nop 0
	s_nop 0
	s_nop 0
	s_nop 0
	s_nop 0
	s_nop 0
	s_nop 0
	s_nop 0
	s_nop 0
	s_nop 0
	s_nop 0
	s_nop 0
	s_nop 0
	s_nop 0
	s_nop 0
	s_nop 0
	s_nop 0
	s_nop 0
	s_nop 0
	s_nop 0
	s_nop 0
	s_nop 0
	s_nop 0
	s_nop 0
	s_nop 0
	s_nop 0
	s_nop 0
	s_nop 0
	s_nop 0
	s_nop 0
	s_nop 0
	s_nop 0
	s_nop 0
	s_nop 0
	s_nop 0
	s_nop 0
	s_nop 0
	s_nop 0
	s_nop 0
	s_nop 0
	s_nop 0
	s_nop 0
	s_nop 0
	s_nop 0
	s_nop 0
	s_nop 0
	s_nop 0
	s_nop 0
	s_nop 0
	s_nop 0
	s_nop 0
	s_nop 0
	s_nop 0
	s_nop 0
	s_nop 0
	s_nop 0
	s_nop 0
	s_nop 0
	s_nop 0
	s_nop 0
	s_nop 0
	s_nop 0
	s_nop 0
	s_nop 0
	s_nop 0
	s_nop 0
	s_nop 0
	s_nop 0
	s_nop 0
	s_nop 0
	s_nop 0
	s_nop 0
	s_nop 0
	s_nop 0
	s_nop 0
	s_nop 0
	s_nop 0
	s_nop 0
	s_nop 0
	s_nop 0
	s_nop 0
	s_nop 0
	s_nop 0
	s_nop 0
	s_nop 0
	s_nop 0
	s_nop 0
	s_nop 0
	s_nop 0
	s_nop 0
	s_nop 0
	s_nop 0
	s_nop 0
	s_nop 0
	s_nop 0
	s_nop 0
	s_nop 0
	s_nop 0
	s_nop 0
	s_nop 0
	s_nop 0
	s_nop 0
	s_nop 0
	s_nop 0
	s_nop 0
	s_nop 0
	s_nop 0
	s_nop 0
	s_nop 0
	s_nop 0
	s_nop 0
	s_nop 0
	s_nop 0
	s_nop 0
	s_nop 0
	s_nop 0
	s_nop 0
	s_nop 0
	s_nop 0
	s_nop 0
	s_nop 0
	s_nop 0
	s_nop 0
	s_nop 0
	s_nop 0
	s_nop 0
	s_nop 0
	s_nop 0
	s_nop 0
	s_nop 0
	s_nop 0
	s_nop 0
	s_nop 0
	s_nop 0
	s_nop 0
	s_nop 0
	s_nop 0
	s_nop 0
	s_nop 0
	s_nop 0
	s_nop 0
	s_nop 0
	s_nop 0
	s_nop 0
	s_nop 0
	s_nop 0
	s_nop 0
	s_nop 0
	s_nop 0
	s_nop 0
	s_nop 0
	s_nop 0
	s_nop 0
	s_nop 0
	s_nop 0
	s_nop 0
	s_nop 0
	s_nop 0
	s_nop 0
	s_nop 0
	s_nop 0
	s_nop 0
	s_nop 0
	s_nop 0
	s_nop 0
	s_nop 0
	s_nop 0
	s_nop 0
	s_nop 0
	s_nop 0
	s_nop 0
	s_nop 0
	s_nop 0
	s_nop 0
	s_nop 0
	s_nop 0
	s_nop 0
	s_nop 0
	s_nop 0
	s_nop 0
	s_nop 0
	s_nop 0
	s_nop 0
	s_nop 0
	s_nop 0
	s_nop 0
	s_nop 0
	s_nop 0
	s_nop 0
	s_nop 0
	s_nop 0
	s_nop 0
	s_nop 0
	s_nop 0
	s_nop 0
	s_nop 0
	s_nop 0
	s_nop 0
	s_nop 0
	s_nop 0
	s_nop 0
	s_nop 0
	s_nop 0
	s_nop 0
	s_nop 0
	s_nop 0
	s_nop 0
	s_nop 0
	s_nop 0
	s_nop 0
	s_nop 0
	s_nop 0
	s_nop 0
	s_nop 0
	s_nop 0
	s_nop 0
	s_nop 0
	s_nop 0
	s_nop 0
	s_nop 0
	s_nop 0
	s_nop 0
	s_nop 0
	s_nop 0
	s_nop 0
	s_nop 0
	s_nop 0
	s_nop 0
	s_nop 0
	s_nop 0
	s_nop 0
	s_nop 0
	s_nop 0
	s_nop 0
	s_nop 0
	s_nop 0
	s_nop 0
	s_nop 0
	s_nop 0
	s_nop 0
	s_nop 0
	s_nop 0
	s_nop 0
	s_nop 0
	s_nop 0
	s_nop 0
	s_nop 0
	s_nop 0
	s_nop 0
	s_nop 0
	s_nop 0
	s_nop 0
	s_nop 0
	s_nop 0
	s_nop 0
	s_nop 0
	s_nop 0
	s_nop 0
	s_nop 0
	s_nop 0
	s_nop 0
	s_nop 0
	s_nop 0
	s_nop 0
	s_nop 0
	s_nop 0
	s_nop 0
	s_nop 0
	s_nop 0
	s_nop 0
	s_nop 0
	s_nop 0
	s_nop 0
	s_nop 0
	s_nop 0
	s_nop 0
	s_nop 0
	s_nop 0
	s_nop 0
	s_nop 0
	s_nop 0
	s_nop 0
	s_nop 0
	s_nop 0
	s_nop 0
	s_nop 0
	s_nop 0
	s_nop 0
	s_nop 0
	s_nop 0
	s_nop 0
	s_nop 0
	s_nop 0
	s_nop 0
	s_nop 0
	s_nop 0
	s_nop 0
	s_nop 0
	s_nop 0
	s_nop 0
	s_nop 0
	s_nop 0
	s_nop 0
	s_nop 0
	s_nop 0
	s_nop 0
	s_nop 0
	s_nop 0
	s_nop 0
	s_nop 0
	s_nop 0
	s_nop 0
	s_nop 0
	s_nop 0
	s_nop 0
	s_nop 0
	s_nop 0
	s_nop 0
	s_nop 0
	s_nop 0
	s_nop 0
	s_nop 0
	s_nop 0
	s_nop 0
	s_nop 0
	s_nop 0
	s_nop 0
	s_nop 0
	s_nop 0
	s_nop 0
	s_nop 0
	s_nop 0
	s_nop 0
	s_nop 0
	s_nop 0
	s_nop 0
	s_nop 0
	s_nop 0
	s_nop 0
	s_nop 0
	s_nop 0
	s_nop 0
	s_nop 0
	s_nop 0
	s_nop 0
	s_nop 0
	s_nop 0
	s_nop 0
	s_nop 0
	s_nop 0
	s_nop 0
	s_nop 0
	s_nop 0
	s_nop 0
	s_nop 0
	s_nop 0
	s_nop 0
	s_nop 0
	s_nop 0
	s_nop 0
	s_nop 0
	s_nop 0
	s_nop 0
	s_nop 0
	s_nop 0
	s_nop 0
	s_nop 0
	s_nop 0
	s_nop 0
	s_nop 0
	s_nop 0
	s_nop 0
	s_nop 0
	s_nop 0
	s_nop 0
	s_nop 0
	s_nop 0
	s_nop 0
	s_nop 0
	s_nop 0
	s_nop 0
	s_nop 0
	s_nop 0
	s_nop 0
	s_nop 0
	s_nop 0
	s_nop 0
	s_nop 0
	s_nop 0
	s_nop 0
	s_nop 0
	s_nop 0
	s_nop 0
	s_nop 0
	s_nop 0
	s_nop 0
	s_nop 0
	s_nop 0
	s_nop 0
	s_nop 0
	s_nop 0
	s_nop 0
	s_nop 0
	s_nop 0
	s_nop 0
	s_nop 0
	s_nop 0
	s_nop 0
	s_nop 0
	s_nop 0
	s_nop 0
	s_nop 0
	s_nop 0
	s_nop 0
	s_nop 0
	s_nop 0
	s_nop 0
	s_nop 0
	s_nop 0
	s_nop 0
	s_nop 0
	s_nop 0
	s_nop 0
	s_nop 0
	s_nop 0
	s_nop 0
	s_nop 0
	s_nop 0
	s_nop 0
	s_nop 0
	s_nop 0
	s_nop 0
	s_nop 0
	s_nop 0
	s_nop 0
	s_nop 0
	s_nop 0
	s_nop 0
	s_nop 0
	s_nop 0
	s_nop 0
	s_nop 0
	s_nop 0
	s_nop 0
	s_nop 0
	s_nop 0
	s_nop 0
	s_nop 0
	s_nop 0
	s_nop 0
	s_nop 0
	s_nop 0
	s_nop 0
	s_nop 0
	s_nop 0
	s_nop 0
	s_nop 0
	s_nop 0
	s_nop 0
	s_nop 0
	s_nop 0
	s_nop 0
	s_nop 0
	s_nop 0
	s_nop 0
	s_nop 0
	s_nop 0
	s_nop 0
	s_nop 0
	s_nop 0
	s_nop 0
	s_nop 0
	s_nop 0
	s_nop 0
	s_nop 0
	s_nop 0
	s_nop 0
	s_nop 0
	s_nop 0
	s_nop 0
	s_nop 0
	s_nop 0
	s_nop 0
	s_nop 0
	s_nop 0
	s_nop 0
	s_nop 0
	s_nop 0
	s_nop 0
	s_nop 0
	s_nop 0
	s_nop 0
	s_nop 0
	s_nop 0
	s_nop 0
	s_nop 0
	s_nop 0
	s_nop 0
	s_nop 0
	s_nop 0
	s_nop 0
	s_nop 0
	s_nop 0
	s_nop 0
	s_nop 0
	s_nop 0
	s_nop 0
	s_nop 0
	s_nop 0
	s_nop 0
	s_nop 0
	s_nop 0
	s_nop 0
	s_nop 0
; __device__ __forceinline__ CArgs cargs() { CArgs p = (CArgs)__builtin_amdgcn_kernarg_segment_ptr(); asm volatile("" : "+s"(p)); return p; }
; #define GRID_BAR_T(FIRST) do { XcdBarrier bb; bb.bar = (unsigned*)(cargs()->ws + WS_CTL) + CW_BAR; bb.x = xb_xcc_id(); bb.st = (volatile LAS unsigned*)(lds + MISC_OFF); \
;         xcd_barrier<FIRST>(bb, phase_tid(wv) == 0); } while (0)
; #define GRID_BAR_T(FIRST) do {} while (0)
; __global__ void __launch_bounds__(NTHR, 2) mk_fwd(Args a) {
;     ...
;     if (PM(0) && IN(0)) { phase_convert(cargs(), lds, wv); phase_convert_b(cargs(), lds, wv); }
;     if (IN(0) && IN(2)) GRID_BAR_T(true);
	s_nop 0
	s_nop 0
	s_nop 0
	s_nop 0
	s_nop 0
	s_nop 0
	s_nop 0
	s_nop 0
	s_nop 0
	s_nop 0
	s_nop 0
	s_nop 0
	s_nop 0
	s_nop 0
	s_nop 0
	s_nop 0
	s_nop 0
	s_nop 0
	s_nop 0
	s_nop 0
	s_nop 0
	s_nop 0
	s_nop 0
	s_nop 0
	s_nop 0
	s_nop 0
	s_nop 0
	s_nop 0
	s_nop 0
	s_nop 0
	s_nop 0
	s_nop 0
	s_nop 0
	s_nop 0
	s_nop 0
	s_nop 0
	s_nop 0
	s_nop 0
	s_nop 0
	s_nop 0
	s_nop 0
	s_nop 0
	s_nop 0
	s_nop 0
	s_nop 0
	s_nop 0
	s_nop 0
	s_nop 0
	s_nop 0
	s_nop 0
	s_nop 0
	s_nop 0
	s_nop 0
	s_nop 0
	s_nop 0
	s_nop 0
	s_nop 0
	s_nop 0
	s_nop 0
	s_nop 0
	s_nop 0
	s_nop 0
	s_nop 0
	s_nop 0
	s_nop 0
	s_nop 0
	s_nop 0
	s_nop 0
	s_nop 0
	s_nop 0
	s_nop 0
	s_nop 0
	s_nop 0
	s_nop 0
	s_nop 0
	s_nop 0
	s_nop 0
	s_nop 0
	s_nop 0
	s_nop 0
	s_nop 0
	s_nop 0
	s_nop 0
	s_nop 0
	s_nop 0
	s_nop 0
	s_nop 0
	s_nop 0
	s_nop 0
	s_nop 0
	s_nop 0
	s_nop 0
	s_nop 0
	s_nop 0
	s_nop 0
	s_nop 0
	s_nop 0
	s_nop 0
	s_nop 0
	s_nop 0
	s_nop 0
	s_nop 0
	s_nop 0
	s_nop 0
	s_nop 0
	s_nop 0
	s_nop 0
	s_nop 0
	s_nop 0
	s_nop 0
	s_nop 0
	s_nop 0
	s_nop 0
	s_nop 0
	s_nop 0
	s_nop 0
	s_nop 0
	s_nop 0
	s_nop 0
	s_nop 0
	s_nop 0
	s_nop 0
	s_nop 0
	s_nop 0
	s_nop 0
	s_nop 0
	s_nop 0
	s_nop 0
	s_nop 0
	s_nop 0
	s_nop 0
	s_nop 0
	s_nop 0
	s_nop 0
	s_nop 0
	s_nop 0
	s_nop 0
	s_nop 0
	s_nop 0
	s_nop 0
	s_nop 0
	s_nop 0
	s_nop 0
	s_nop 0
	s_nop 0
	s_nop 0
	s_nop 0
	s_nop 0
	s_nop 0
	s_nop 0
	s_nop 0
	s_nop 0
	s_nop 0
	s_nop 0
	s_nop 0
	s_nop 0
	s_nop 0
	s_nop 0
	s_nop 0
	s_nop 0
	s_nop 0
	s_nop 0
	s_nop 0
	s_nop 0
	s_nop 0
	s_nop 0
	s_nop 0
	s_nop 0
	s_nop 0
	s_nop 0
	s_nop 0
	s_nop 0
	s_nop 0
	s_nop 0
	s_nop 0
	s_nop 0
	s_nop 0
	s_nop 0
	s_nop 0
	s_nop 0
	s_nop 0
	s_nop 0
	s_nop 0
	s_nop 0
	s_nop 0
	s_nop 0
	s_nop 0
	s_nop 0
	s_nop 0
	s_nop 0
	s_nop 0
	s_nop 0
	s_nop 0
	s_nop 0
	s_nop 0
	s_nop 0
	s_nop 0
	s_nop 0
	s_nop 0
	s_nop 0
	s_nop 0
	s_nop 0
	s_nop 0
	s_nop 0
	s_nop 0
	s_nop 0
	s_nop 0
	s_nop 0
	s_nop 0
	s_nop 0
	s_nop 0
	s_nop 0
	s_nop 0
	s_nop 0
	s_nop 0
	s_nop 0
	s_nop 0
	s_nop 0
	s_nop 0
	s_nop 0
	s_nop 0
	s_nop 0
	s_nop 0
	s_nop 0
	s_nop 0
	s_nop 0
	s_nop 0
	s_nop 0
	s_nop 0
	s_nop 0
	s_nop 0
	s_nop 0
	s_nop 0
	s_nop 0
	s_nop 0
	s_nop 0
	s_nop 0
	s_nop 0
	s_nop 0
	s_nop 0
	s_nop 0
	s_nop 0
	s_nop 0
	s_nop 0
	s_nop 0
	s_nop 0
	s_nop 0
	s_nop 0
	s_nop 0
	s_nop 0
	s_nop 0
	s_nop 0
	s_nop 0
	s_nop 0
	s_nop 0
	s_nop 0
	s_nop 0
	s_nop 0
	s_nop 0
	s_nop 0
	s_nop 0
	s_nop 0
	s_nop 0
	s_nop 0
	s_nop 0
	s_nop 0
	s_nop 0
	s_nop 0
	s_nop 0
	s_nop 0
	s_nop 0
	s_nop 0
	s_nop 0
	s_nop 0
	s_nop 0
	s_nop 0
	s_nop 0
	s_nop 0
	s_nop 0
	s_nop 0
	s_nop 0
	s_nop 0
	s_nop 0
	s_nop 0
	s_nop 0
	s_nop 0
	s_nop 0
	s_nop 0
	s_nop 0
	s_nop 0
	s_nop 0
	s_nop 0
	s_nop 0
	s_nop 0
	s_nop 0
	s_nop 0
	s_nop 0
	s_nop 0
	s_nop 0
	s_nop 0
	s_nop 0
	s_nop 0
	s_nop 0
	s_nop 0
	s_nop 0
	s_nop 0
	s_nop 0
	s_nop 0
	s_nop 0
	s_nop 0
	s_nop 0
	s_nop 0
	s_nop 0
	s_nop 0
	s_nop 0
	s_nop 0
	s_nop 0
	s_nop 0
	s_nop 0
	s_nop 0
	s_nop 0
	s_nop 0
	s_nop 0
	s_nop 0
	s_nop 0
	s_nop 0
	s_nop 0
	s_nop 0
	s_nop 0
	s_nop 0
	s_nop 0
	s_nop 0
	s_nop 0
	s_nop 0
	s_nop 0
	s_nop 0
	s_nop 0
	s_nop 0
	s_nop 0
	s_nop 0
	s_nop 0
	s_nop 0
	s_nop 0
	s_nop 0
	s_nop 0
	s_nop 0
	s_nop 0
	s_nop 0
	s_nop 0
	s_nop 0
	s_nop 0
	s_nop 0
	s_nop 0
	s_nop 0
	s_nop 0
	s_nop 0
	s_nop 0
	s_nop 0
	s_nop 0
	s_nop 0
	s_nop 0
	s_nop 0
	s_nop 0
	s_nop 0
	s_nop 0
	s_nop 0
	s_nop 0
	s_nop 0
	s_nop 0
	s_nop 0
	s_nop 0
	s_nop 0
	s_nop 0
	s_nop 0
	s_nop 0
	s_nop 0
	s_nop 0
	s_nop 0
	s_nop 0
	s_nop 0
	s_nop 0
	s_nop 0
	s_nop 0
	s_nop 0
	s_nop 0
	s_nop 0
	s_nop 0
	s_nop 0
	s_nop 0
	s_nop 0
	s_nop 0
	s_nop 0
	s_nop 0
	s_nop 0
	s_nop 0
	s_nop 0
	s_nop 0
	s_nop 0
	s_nop 0
	s_nop 0
	s_nop 0
	s_nop 0
	s_nop 0
	s_nop 0
	s_nop 0
	s_nop 0
	s_nop 0
	s_nop 0
	s_nop 0
	s_nop 0
	s_nop 0
	s_nop 0
	s_nop 0
	s_nop 0
	s_nop 0
	s_nop 0
	s_nop 0
	s_nop 0
	s_nop 0
	s_nop 0
	s_nop 0
	s_nop 0
	s_nop 0
	s_nop 0
	s_nop 0
	s_nop 0
	s_nop 0
	s_nop 0
	s_nop 0
	s_nop 0
	s_nop 0
	s_nop 0
	s_nop 0
	s_nop 0
	s_nop 0
	s_nop 0
	s_nop 0
	s_nop 0
	s_nop 0
	s_nop 0
	s_nop 0
	s_nop 0
	s_nop 0
	s_nop 0
	s_nop 0
	s_nop 0
	s_nop 0
	s_nop 0
	s_nop 0
	s_nop 0
	s_nop 0
	s_nop 0
	s_nop 0
	s_nop 0
	s_nop 0
	s_nop 0
	s_nop 0
	s_nop 0
	s_nop 0
	s_nop 0
	s_nop 0
	s_nop 0
	s_nop 0
	s_nop 0
	s_nop 0
	s_nop 0
	s_nop 0
	s_nop 0
	s_nop 0
	s_nop 0
	s_nop 0
	s_nop 0
	s_nop 0
	s_nop 0
	s_nop 0
	s_nop 0
	s_nop 0
	s_nop 0
	s_nop 0
	s_nop 0
	s_nop 0
	s_nop 0
	s_nop 0
	s_nop 0
	s_nop 0
	s_nop 0
	s_nop 0
	s_nop 0
	s_nop 0
	s_nop 0
	s_nop 0
	s_nop 0
	s_nop 0
	s_nop 0
	s_nop 0
	s_nop 0
	s_nop 0
	s_nop 0
	s_nop 0
	s_nop 0
	s_nop 0
	s_nop 0
	s_nop 0
	s_nop 0
	s_nop 0
	s_nop 0
	s_nop 0
	s_nop 0
	s_nop 0
	s_nop 0
	s_nop 0
	s_nop 0
	s_nop 0
	s_nop 0
	s_nop 0
	s_nop 0
	s_nop 0
	s_nop 0
	s_nop 0
	s_nop 0
	s_nop 0
	s_nop 0
	s_nop 0
	s_nop 0
	s_nop 0
	s_nop 0
	s_nop 0
	s_nop 0
	s_nop 0
	s_nop 0
	s_nop 0
	s_nop 0
	s_nop 0
	s_nop 0
	s_nop 0
	s_nop 0
	s_nop 0
	s_nop 0
	s_nop 0
	s_nop 0
	s_nop 0
	s_nop 0
	s_nop 0
	s_nop 0
	s_nop 0
	s_nop 0
	s_nop 0
	s_nop 0
	s_nop 0
	s_nop 0
	s_nop 0
	s_nop 0
	s_nop 0
	s_nop 0
	s_nop 0
	s_nop 0
	s_nop 0
	s_nop 0
	s_nop 0
	s_nop 0
	s_nop 0
	s_nop 0
	s_nop 0
	s_nop 0
	s_nop 0
	s_nop 0
	s_nop 0
	s_nop 0
	s_nop 0
	s_nop 0
	s_nop 0
	s_nop 0
	s_nop 0
	s_nop 0
	s_nop 0
	s_nop 0
	s_nop 0
	s_nop 0
	s_nop 0
	s_nop 0
	s_nop 0
	s_nop 0
	s_nop 0
	s_nop 0
	s_nop 0
	s_nop 0
	s_nop 0
	s_nop 0
	s_nop 0
	s_nop 0
	s_nop 0
	s_nop 0
	s_nop 0
	s_nop 0
	s_nop 0
	s_nop 0
	s_nop 0
	s_nop 0
	s_nop 0
	s_nop 0
	s_nop 0
	s_nop 0
	s_nop 0
	s_nop 0
	s_nop 0
	s_nop 0
	s_nop 0
	s_nop 0
	s_nop 0
	s_nop 0
	s_nop 0
	s_nop 0
	s_nop 0
	s_nop 0
	s_nop 0
	s_nop 0
	s_nop 0
	s_nop 0
	s_nop 0
	s_nop 0
	s_nop 0
	s_nop 0
	s_nop 0
	s_nop 0
	s_nop 0
	s_nop 0
	s_nop 0
; __device__ __forceinline__ CArgs cargs() { CArgs p = (CArgs)__builtin_amdgcn_kernarg_segment_ptr(); asm volatile("" : "+s"(p)); return p; }
; #define GRID_BAR_T(FIRST) do { XcdBarrier bb; bb.bar = (unsigned*)(cargs()->ws + WS_CTL) + CW_BAR; bb.x = xb_xcc_id(); bb.st = (volatile LAS unsigned*)(lds + MISC_OFF); \
;         xcd_barrier<FIRST>(bb, phase_tid(wv) == 0); } while (0)
; #define GRID_BAR_T(FIRST) do {} while (0)
; __global__ void __launch_bounds__(NTHR, 2) mk_fwd(Args a) {
;     ...
;     if (PM(0) && IN(0)) { phase_convert(cargs(), lds, wv); phase_convert_b(cargs(), lds, wv); }
;     if (IN(0) && IN(2)) GRID_BAR_T(true);
	s_nop 0
	s_nop 0
	s_nop 0
	s_nop 0
	s_nop 0
	s_nop 0
	s_nop 0
	s_nop 0
	s_nop 0
	s_nop 0
	s_nop 0
	s_nop 0
	s_nop 0
	s_nop 0
	s_nop 0
	s_nop 0
	s_nop 0
	s_nop 0
	s_nop 0
	s_nop 0
	s_nop 0
	s_nop 0
	s_nop 0
	s_nop 0
	s_nop 0
	s_nop 0
	s_nop 0
	s_nop 0
	s_nop 0
	s_nop 0
	s_nop 0
	s_nop 0
	s_nop 0
	s_nop 0
	s_nop 0
	s_nop 0
	s_nop 0
	s_nop 0
	s_nop 0
	s_nop 0
	s_nop 0
	s_nop 0
	s_nop 0
	s_nop 0
	s_nop 0
	s_nop 0
	s_nop 0
	s_nop 0
	s_nop 0
	s_nop 0
	s_nop 0
	s_nop 0
	s_nop 0
	s_nop 0
	s_nop 0
	s_nop 0
	s_nop 0
	s_nop 0
	s_nop 0
	s_nop 0
	s_nop 0
	s_nop 0
	s_nop 0
	s_nop 0
	s_nop 0
	s_nop 0
	s_nop 0
	s_nop 0
	s_nop 0
	s_nop 0
	s_nop 0
	s_nop 0
	s_nop 0
	s_nop 0
	s_nop 0
	s_nop 0
	s_nop 0
	s_nop 0
	s_nop 0
	s_nop 0
	s_nop 0
	s_nop 0
	s_nop 0
	s_nop 0
	s_nop 0
	s_nop 0
	s_nop 0
	s_nop 0
	s_nop 0
	s_nop 0
	s_nop 0
	s_nop 0
	s_nop 0
	s_nop 0
	s_nop 0
	s_nop 0
	s_nop 0
	s_nop 0
	s_nop 0
	s_nop 0
	s_nop 0
	s_nop 0
	s_nop 0
	s_nop 0
	s_nop 0
	s_nop 0
	s_nop 0
	s_nop 0
	s_nop 0
	s_nop 0
	s_nop 0
	s_nop 0
	s_nop 0
	s_nop 0
	s_nop 0
	s_nop 0
	s_nop 0
	s_nop 0
	s_nop 0
	s_nop 0
	s_nop 0
	s_nop 0
	s_nop 0
	s_nop 0
	s_nop 0
	s_nop 0
	s_nop 0
	s_nop 0
	s_nop 0
	s_nop 0
	s_nop 0
	s_nop 0
	s_nop 0
	s_nop 0
	s_nop 0
	s_nop 0
	s_nop 0
	s_nop 0
	s_nop 0
	s_nop 0
	s_nop 0
	s_nop 0
	s_nop 0
	s_nop 0
	s_nop 0
	s_nop 0
	s_nop 0
	s_nop 0
	s_nop 0
	s_nop 0
	s_nop 0
	s_nop 0
	s_nop 0
	s_nop 0
	s_nop 0
	s_nop 0
	s_nop 0
	s_nop 0
	s_nop 0
	s_nop 0
	s_nop 0
	s_nop 0
	s_nop 0
	s_nop 0
	s_nop 0
	s_nop 0
	s_nop 0
	s_nop 0
	s_nop 0
	s_nop 0
	s_nop 0
	s_nop 0
	s_nop 0
	s_nop 0
	s_nop 0
	s_nop 0
	s_nop 0
	s_nop 0
	s_nop 0
	s_nop 0
	s_nop 0
	s_nop 0
	s_nop 0
	s_nop 0
	s_nop 0
	s_nop 0
	s_nop 0
	s_nop 0
	s_nop 0
	s_nop 0
	s_nop 0
	s_nop 0
	s_nop 0
	s_nop 0
	s_nop 0
	s_nop 0
	s_nop 0
	s_nop 0
	s_nop 0
	s_nop 0
	s_nop 0
	s_nop 0
	s_nop 0
	s_nop 0
	s_nop 0
	s_nop 0
	s_nop 0
	s_nop 0
	s_nop 0
	s_nop 0
	s_nop 0
	s_nop 0
	s_nop 0
	s_nop 0
	s_nop 0
	s_nop 0
	s_nop 0
	s_nop 0
	s_nop 0
	s_nop 0
	s_nop 0
	s_nop 0
	s_nop 0
	s_nop 0
	s_nop 0
	s_nop 0
	s_nop 0
	s_nop 0
	s_nop 0
	s_nop 0
	s_nop 0
	s_nop 0
	s_nop 0
	s_nop 0
	s_nop 0
	s_nop 0
	s_nop 0
	s_nop 0
	s_nop 0
	s_nop 0
	s_nop 0
	s_nop 0
	s_nop 0
	s_nop 0
	s_nop 0
	s_nop 0
	s_nop 0
	s_nop 0
	s_nop 0
	s_nop 0
	s_nop 0
	s_nop 0
	s_nop 0
	s_nop 0
	s_nop 0
	s_nop 0
	s_nop 0
	s_nop 0
	s_nop 0
	s_nop 0
	s_nop 0
	s_nop 0
	s_nop 0
	s_nop 0
	s_nop 0
	s_nop 0
	s_nop 0
	s_nop 0
	s_nop 0
	s_nop 0
	s_nop 0
	s_nop 0
	s_nop 0
	s_nop 0
	s_nop 0
	s_nop 0
	s_nop 0
	s_nop 0
	s_nop 0
	s_nop 0
	s_nop 0
	s_nop 0
	s_nop 0
	s_nop 0
	s_nop 0
	s_nop 0
	s_nop 0
	s_nop 0
	s_nop 0
	s_nop 0
	s_nop 0
	s_nop 0
	s_nop 0
	s_nop 0
	s_nop 0
	s_nop 0
	s_nop 0
	s_nop 0
	s_nop 0
	s_nop 0
	s_nop 0
	s_nop 0
	s_nop 0
	s_nop 0
	s_nop 0
	s_nop 0
	s_nop 0
	s_nop 0
	s_nop 0
	s_nop 0
	s_nop 0
	s_nop 0
	s_nop 0
	s_nop 0
	s_nop 0
	s_nop 0
	s_nop 0
	s_nop 0
	s_nop 0
	s_nop 0
	s_nop 0
	s_nop 0
	s_nop 0
	s_nop 0
	s_nop 0
	s_nop 0
	s_nop 0
	s_nop 0
	s_nop 0
	s_nop 0
	s_nop 0
	s_nop 0
	s_nop 0
	s_nop 0
	s_nop 0
	s_nop 0
	s_nop 0
	s_nop 0
	s_nop 0
	s_nop 0
	s_nop 0
	s_nop 0
	s_nop 0
	s_nop 0
	s_nop 0
	s_nop 0
	s_nop 0
	s_nop 0
	s_nop 0
	s_nop 0
	s_nop 0
	s_nop 0
	s_nop 0
	s_nop 0
	s_nop 0
	s_nop 0
	s_nop 0
	s_nop 0
	s_nop 0
	s_nop 0
	s_nop 0
	s_nop 0
	s_nop 0
	s_nop 0
	s_nop 0
	s_nop 0
	s_nop 0
	s_nop 0
	s_nop 0
	s_nop 0
	s_nop 0
	s_nop 0
	s_nop 0
	s_nop 0
	s_nop 0
	s_nop 0
	s_nop 0
	s_nop 0
	s_nop 0
	s_nop 0
	s_nop 0
	s_nop 0
	s_nop 0
	s_nop 0
	s_nop 0
	s_nop 0
	s_nop 0
	s_nop 0
	s_nop 0
	s_nop 0
	s_nop 0
	s_nop 0
	s_nop 0
	s_nop 0
	s_nop 0
	s_nop 0
	s_nop 0
	s_nop 0
	s_nop 0
	s_nop 0
	s_nop 0
	s_nop 0
	s_nop 0
	s_nop 0
	s_nop 0
	s_nop 0
	s_nop 0
	s_nop 0
	s_nop 0
	s_nop 0
	s_nop 0
	s_nop 0
	s_nop 0
	s_nop 0
	s_nop 0
	s_nop 0
	s_nop 0
	s_nop 0
	s_nop 0
	s_nop 0
	s_nop 0
	s_nop 0
	s_nop 0
	s_nop 0
	s_nop 0
	s_nop 0
	s_nop 0
	s_nop 0
	s_nop 0
	s_nop 0
	s_nop 0
	s_nop 0
	s_nop 0
	s_nop 0
	s_nop 0
	s_nop 0
	s_nop 0
	s_nop 0
	s_nop 0
	s_nop 0
	s_nop 0
	s_nop 0
	s_nop 0
	s_nop 0
	s_nop 0
	s_nop 0
	s_nop 0
	s_nop 0
	s_nop 0
	s_nop 0
	s_nop 0
	s_nop 0
	s_nop 0
	s_nop 0
	s_nop 0
	s_nop 0
	s_nop 0
	s_nop 0
	s_nop 0
	s_nop 0
	s_nop 0
	s_nop 0
	s_nop 0
	s_nop 0
	s_nop 0
	s_nop 0
	s_nop 0
	s_nop 0
	s_nop 0
	s_nop 0
	s_nop 0
	s_nop 0
	s_nop 0
	s_nop 0
	s_nop 0
	s_nop 0
	s_nop 0
	s_nop 0
	s_nop 0
	s_nop 0
	s_nop 0
	s_nop 0
	s_nop 0
	s_nop 0
	s_nop 0
	s_nop 0
	s_nop 0
	s_nop 0
	s_nop 0
	s_nop 0
	s_nop 0
	s_nop 0
	s_nop 0
	s_nop 0
	s_nop 0
	s_nop 0
	s_nop 0
	s_nop 0
	s_nop 0
	s_nop 0
	s_nop 0
	s_nop 0
	s_nop 0
	s_nop 0
	s_nop 0
	s_nop 0
	s_nop 0
	s_nop 0
	s_nop 0
	s_nop 0
	s_nop 0
	s_nop 0
	s_nop 0
	s_nop 0
	s_nop 0
	s_nop 0
	s_nop 0
	s_nop 0
	s_nop 0
	s_nop 0
	s_nop 0
	s_nop 0
	s_nop 0
	s_nop 0
	s_nop 0
	s_nop 0
	s_nop 0
	s_nop 0
	s_nop 0
	s_nop 0
	s_nop 0
	s_nop 0
	s_nop 0
	s_nop 0
	s_nop 0
	s_nop 0
	s_nop 0
	s_nop 0
	s_nop 0
	s_nop 0
	s_nop 0
	s_nop 0
	s_nop 0
	s_nop 0
	s_nop 0
	s_nop 0
	s_nop 0
	s_nop 0
	s_nop 0
	s_nop 0
	s_nop 0
	s_nop 0
	s_nop 0
	s_nop 0
	s_nop 0
	s_nop 0
	s_nop 0
	s_nop 0
	s_nop 0
	s_nop 0
	s_nop 0
	s_nop 0
	s_nop 0
	s_nop 0
	s_nop 0
	s_nop 0
	s_nop 0
	s_nop 0
	s_nop 0
	s_nop 0
	s_nop 0
	s_nop 0
	s_nop 0
	s_nop 0
	s_nop 0
	s_nop 0
	s_nop 0
	s_nop 0
	s_nop 0
	s_nop 0
	s_nop 0
	s_nop 0
	s_nop 0
	s_nop 0
	s_nop 0
	s_nop 0
	s_nop 0
	s_nop 0
	s_nop 0
	s_nop 0
	s_nop 0
	s_nop 0
	s_nop 0
	s_nop 0
	s_nop 0
	s_nop 0
	s_nop 0
	s_nop 0
	s_nop 0
	s_nop 0
	s_nop 0
	s_nop 0
	s_nop 0
	s_nop 0
	s_nop 0
	s_nop 0
	s_nop 0
	s_nop 0
	s_nop 0
	s_nop 0
	s_nop 0
	s_nop 0
	s_nop 0
	s_nop 0
	s_nop 0
	s_nop 0
	s_nop 0
	s_nop 0
	s_nop 0
	s_nop 0
	s_nop 0
	s_nop 0
	s_nop 0
	s_nop 0
	s_nop 0
	s_nop 0
	s_nop 0
; __device__ __forceinline__ CArgs cargs() { CArgs p = (CArgs)__builtin_amdgcn_kernarg_segment_ptr(); asm volatile("" : "+s"(p)); return p; }
; #define GRID_BAR_T(FIRST) do { XcdBarrier bb; bb.bar = (unsigned*)(cargs()->ws + WS_CTL) + CW_BAR; bb.x = xb_xcc_id(); bb.st = (volatile LAS unsigned*)(lds + MISC_OFF); \
;         xcd_barrier<FIRST>(bb, phase_tid(wv) == 0); } while (0)
; #define GRID_BAR_T(FIRST) do {} while (0)
; __global__ void __launch_bounds__(NTHR, 2) mk_fwd(Args a) {
;     ...
;     if (PM(0) && IN(0)) { phase_convert(cargs(), lds, wv); phase_convert_b(cargs(), lds, wv); }
;     if (IN(0) && IN(2)) GRID_BAR_T(true);
	s_nop 0
	s_nop 0
	s_nop 0
	s_nop 0
	s_nop 0
	s_nop 0
	s_nop 0
	s_nop 0
	s_nop 0
	s_nop 0
	s_nop 0
	s_nop 0
	s_nop 0
	s_nop 0
	s_nop 0
	s_nop 0
	s_nop 0
	s_nop 0
	s_nop 0
	s_nop 0
	s_nop 0
	s_nop 0
	s_nop 0
	s_nop 0
	s_nop 0
	s_nop 0
	s_nop 0
	s_nop 0
	s_nop 0
	s_nop 0
	s_nop 0
	s_nop 0
	s_nop 0
	s_nop 0
	s_nop 0
	s_nop 0
	s_nop 0
	s_nop 0
	s_nop 0
	s_nop 0
	s_nop 0
	s_nop 0
	s_nop 0
	s_nop 0
	s_nop 0
	s_nop 0
	s_nop 0
	s_nop 0
	s_nop 0
	s_nop 0
	s_nop 0
	s_nop 0
	s_nop 0
	s_nop 0
	s_nop 0
	s_nop 0
	s_nop 0
	s_nop 0
	s_nop 0
	s_nop 0
	s_nop 0
	s_nop 0
	s_nop 0
	s_nop 0
	s_nop 0
	s_nop 0
	s_nop 0
	s_nop 0
	s_nop 0
	s_nop 0
	s_nop 0
	s_nop 0
	s_nop 0
	s_nop 0
	s_nop 0
	s_nop 0
	s_nop 0
	s_nop 0
	s_nop 0
	s_nop 0
	s_nop 0
	s_nop 0
	s_nop 0
	s_nop 0
	s_nop 0
	s_nop 0
	s_nop 0
	s_nop 0
	s_nop 0
	s_nop 0
	s_nop 0
	s_nop 0
	s_nop 0
	s_nop 0
	s_nop 0
	s_nop 0
	s_nop 0
	s_nop 0
	s_nop 0
	s_nop 0
	s_nop 0
	s_nop 0
	s_nop 0
	s_nop 0
	s_nop 0
	s_nop 0
	s_nop 0
	s_nop 0
	s_nop 0
	s_nop 0
	s_nop 0
	s_nop 0
	s_nop 0
	s_nop 0
	s_nop 0
	s_nop 0
	s_nop 0
	s_nop 0
	s_nop 0
	s_nop 0
	s_nop 0
	s_nop 0
	s_nop 0
	s_nop 0
	s_nop 0
	s_nop 0
	s_nop 0
	s_nop 0
	s_nop 0
	s_nop 0
	s_nop 0
	s_nop 0
	s_nop 0
	s_nop 0
	s_nop 0
	s_nop 0
	s_nop 0
	s_nop 0
	s_nop 0
	s_nop 0
	s_nop 0
	s_nop 0
	s_nop 0
	s_nop 0
	s_nop 0
	s_nop 0
	s_nop 0
	s_nop 0
	s_nop 0
	s_nop 0
	s_nop 0
	s_nop 0
	s_nop 0
	s_nop 0
	s_nop 0
	s_nop 0
	s_nop 0
	s_nop 0
	s_nop 0
	s_nop 0
	s_nop 0
	s_nop 0
	s_nop 0
	s_nop 0
	s_nop 0
	s_nop 0
	s_nop 0
	s_nop 0
	s_nop 0
	s_nop 0
	s_nop 0
	s_nop 0
	s_nop 0
	s_nop 0
	s_nop 0
	s_nop 0
	s_nop 0
	s_nop 0
	s_nop 0
	s_nop 0
	s_nop 0
	s_nop 0
	s_nop 0
	s_nop 0
	s_nop 0
	s_nop 0
	s_nop 0
	s_nop 0
	s_nop 0
	s_nop 0
	s_nop 0
	s_nop 0
	s_nop 0
	s_nop 0
	s_nop 0
	s_nop 0
	s_nop 0
	s_nop 0
	s_nop 0
	s_nop 0
	s_nop 0
	s_nop 0
	s_nop 0
	s_nop 0
	s_nop 0
	s_nop 0
	s_nop 0
	s_nop 0
	s_nop 0
	s_nop 0
	s_nop 0
	s_nop 0
	s_nop 0
	s_nop 0
	s_nop 0
	s_nop 0
	s_nop 0
	s_nop 0
	s_nop 0
	s_nop 0
	s_nop 0
	s_nop 0
	s_nop 0
	s_nop 0
	s_nop 0
	s_nop 0
	s_nop 0
	s_nop 0
	s_nop 0
	s_nop 0
	s_nop 0
	s_nop 0
	s_nop 0
	s_nop 0
	s_nop 0
	s_nop 0
	s_nop 0
	s_nop 0
	s_nop 0
	s_nop 0
	s_nop 0
	s_nop 0
	s_nop 0
	s_nop 0
	s_nop 0
	s_nop 0
	s_nop 0
	s_nop 0
	s_nop 0
	s_nop 0
	s_nop 0
	s_nop 0
	s_nop 0
	s_nop 0
	s_nop 0
	s_nop 0
	s_nop 0
	s_nop 0
	s_nop 0
	s_nop 0
	s_nop 0
	s_nop 0
	s_nop 0
	s_nop 0
	s_nop 0
	s_nop 0
	s_nop 0
	s_nop 0
	s_nop 0
	s_nop 0
	s_nop 0
	s_nop 0
	s_nop 0
	s_nop 0
	s_nop 0
	s_nop 0
	s_nop 0
	s_nop 0
	s_nop 0
	s_nop 0
	s_nop 0
	s_nop 0
	s_nop 0
	s_nop 0
	s_nop 0
	s_nop 0
	s_nop 0
	s_nop 0
	s_nop 0
	s_nop 0
	s_nop 0
	s_nop 0
	s_nop 0
	s_nop 0
	s_nop 0
	s_nop 0
	s_nop 0
	s_nop 0
	s_nop 0
	s_nop 0
	s_nop 0
	s_nop 0
	s_nop 0
	s_nop 0
	s_nop 0
	s_nop 0
	s_nop 0
	s_nop 0
	s_nop 0
	s_nop 0
	s_nop 0
	s_nop 0
	s_nop 0
	s_nop 0
	s_nop 0
	s_nop 0
	s_nop 0
	s_nop 0
	s_nop 0
	s_nop 0
	s_nop 0
	s_nop 0
	s_nop 0
	s_nop 0
	s_nop 0
	s_nop 0
	s_nop 0
	s_nop 0
	s_nop 0
	s_nop 0
	s_nop 0
	s_nop 0
	s_nop 0
	s_nop 0
	s_nop 0
	s_nop 0
	s_nop 0
	s_nop 0
	s_nop 0
	s_nop 0
	s_nop 0
	s_nop 0
	s_nop 0
	s_nop 0
	s_nop 0
	s_nop 0
	s_nop 0
	s_nop 0
	s_nop 0
	s_nop 0
	s_nop 0
	s_nop 0
	s_nop 0
	s_nop 0
	s_nop 0
	s_nop 0
	s_nop 0
	s_nop 0
	s_nop 0
	s_nop 0
	s_nop 0
	s_nop 0
	s_nop 0
	s_nop 0
	s_nop 0
	s_nop 0
	s_nop 0
	s_nop 0
	s_nop 0
	s_nop 0
	s_nop 0
	s_nop 0
	s_nop 0
	s_nop 0
	s_nop 0
	s_nop 0
	s_nop 0
	s_nop 0
	s_nop 0
	s_nop 0
	s_nop 0
	s_nop 0
	s_nop 0
	s_nop 0
	s_nop 0
	s_nop 0
	s_nop 0
	s_nop 0
	s_nop 0
	s_nop 0
	s_nop 0
	s_nop 0
	s_nop 0
	s_nop 0
	s_nop 0
	s_nop 0
	s_nop 0
	s_nop 0
	s_nop 0
	s_nop 0
	s_nop 0
	s_nop 0
	s_nop 0
	s_nop 0
	s_nop 0
	s_nop 0
	s_nop 0
	s_nop 0
	s_nop 0
	s_nop 0
	s_nop 0
	s_nop 0
	s_nop 0
	s_nop 0
	s_nop 0
	s_nop 0
	s_nop 0
	s_nop 0
	s_nop 0
	s_nop 0
	s_nop 0
	s_nop 0
	s_nop 0
	s_nop 0
	s_nop 0
	s_nop 0
	s_nop 0
	s_nop 0
	s_nop 0
	s_nop 0
	s_nop 0
	s_nop 0
	s_nop 0
	s_nop 0
	s_nop 0
	s_nop 0
	s_nop 0
	s_nop 0
	s_nop 0
	s_nop 0
	s_nop 0
	s_nop 0
	s_nop 0
	s_nop 0
	s_nop 0
	s_nop 0
	s_nop 0
	s_nop 0
	s_nop 0
	s_nop 0
	s_nop 0
	s_nop 0
	s_nop 0
	s_nop 0
	s_nop 0
	s_nop 0
	s_nop 0
	s_nop 0
	s_nop 0
	s_nop 0
	s_nop 0
	s_nop 0
	s_nop 0
	s_nop 0
	s_nop 0
	s_nop 0
	s_nop 0
	s_nop 0
	s_nop 0
	s_nop 0
	s_nop 0
	s_nop 0
	s_nop 0
	s_nop 0
	s_nop 0
	s_nop 0
	s_nop 0
	s_nop 0
	s_nop 0
	s_nop 0
	s_nop 0
	s_nop 0
	s_nop 0
	s_nop 0
	s_nop 0
	s_nop 0
	s_nop 0
	s_nop 0
	s_nop 0
	s_nop 0
	s_nop 0
	s_nop 0
	s_nop 0
	s_nop 0
	s_nop 0
	s_nop 0
	s_nop 0
	s_nop 0
	s_nop 0
	s_nop 0
	s_nop 0
	s_nop 0
	s_nop 0
	s_nop 0
	s_nop 0
	s_nop 0
	s_nop 0
	s_nop 0
	s_nop 0
	s_nop 0
	s_nop 0
	s_nop 0
	s_nop 0
	s_nop 0
	s_nop 0
	s_nop 0
	s_nop 0
	s_nop 0
	s_nop 0
	s_nop 0
	s_nop 0
	s_nop 0
	s_nop 0
	s_nop 0
	s_nop 0
	s_nop 0
	s_nop 0
	s_nop 0
	s_nop 0
	s_nop 0
	s_nop 0
	s_nop 0
	s_nop 0
	s_nop 0
	s_nop 0
	s_nop 0
	s_nop 0
	s_nop 0
	s_nop 0
	s_nop 0
	s_nop 0
	s_nop 0
	s_nop 0
	s_nop 0
	s_nop 0
	s_nop 0
	s_nop 0
	s_nop 0
	s_nop 0
	s_nop 0
	s_nop 0
	s_nop 0
	s_nop 0
	s_nop 0
	s_nop 0
	s_nop 0
	s_nop 0
	s_nop 0
	s_nop 0
	s_nop 0
	s_nop 0
	s_nop 0
	s_nop 0
	s_nop 0
	s_nop 0
	s_nop 0
	s_nop 0
	s_nop 0
	s_nop 0
	s_nop 0
	s_nop 0
	s_nop 0
	s_nop 0
	s_nop 0
	s_nop 0
	s_nop 0
	s_nop 0
	s_nop 0
	s_nop 0
	s_nop 0
	s_nop 0
	s_nop 0
	s_nop 0
	s_nop 0
	s_nop 0
	s_nop 0
	s_nop 0
	s_nop 0
	s_nop 0
	s_nop 0
	s_nop 0
	s_nop 0
	s_nop 0
	s_nop 0
	s_nop 0
	s_nop 0
	s_nop 0
	s_nop 0
	s_nop 0
	s_nop 0
	s_nop 0
	s_nop 0
	s_nop 0
	s_nop 0
	s_nop 0
	s_nop 0
	s_nop 0
	s_nop 0
	s_nop 0
	s_nop 0
	s_nop 0
	s_nop 0
	s_nop 0
	s_nop 0
	s_nop 0
	s_nop 0
	s_nop 0
	s_nop 0
	s_nop 0
	s_nop 0
	s_nop 0
	s_nop 0
	s_nop 0
	s_nop 0
	s_nop 0
	s_nop 0
	s_nop 0
	s_nop 0
	s_nop 0
	s_nop 0
	s_nop 0
	s_nop 0
	s_nop 0
	s_nop 0
	s_nop 0
	s_nop 0
	s_nop 0
	s_nop 0
	s_nop 0
	s_nop 0
	s_nop 0
	s_nop 0
	s_nop 0
	s_nop 0
	s_nop 0
	s_nop 0
	s_nop 0
	s_nop 0
	s_nop 0
	s_nop 0
	s_nop 0
	s_nop 0
	s_nop 0
	s_nop 0
	s_nop 0
	s_nop 0
	s_nop 0
	s_nop 0
	s_nop 0
	s_nop 0
	s_nop 0
	s_nop 0
	s_nop 0
	s_nop 0
	s_nop 0
	s_nop 0
	s_nop 0
	s_nop 0
	s_nop 0
	s_nop 0
	s_nop 0
	s_nop 0
	s_nop 0
